# P1 k_rope epilogue and P3 q-rope epilogue: rope/ssq quads kept four row groups in flight behind counted waits
# speedup vs baseline: 1.0197x; 1.0197x over previous
; __device__ __forceinline__ u32x4 pack8(f32x4 a, f32x4 b) { u32x4 w; w.x = cvtpk(a[0], a[1]); w.y = cvtpk(a[2], a[3]); w.z = cvtpk(b[0], b[1]); w.w = cvtpk(b[2], b[3]); return w; }
;     __device__ __forceinline__ void operator()(const Acc& acc, const Unit& u, int wr, int wc, int fr, int fq) const {
;     ...
;         } else if (u.col0 == 8192 && wc < 2) {
; #pragma unroll
;             for (int ai = 0; ai < 2; ++ai)
; #pragma unroll
;                 for (int m = 0; m < 4; ++m) { const int row = row0 + ai * HALF + m * 16, pos = row & (SEQ - 1); const int jj = (wc * 32 + 8 * fq) >> 1;
;                     const f32x4 v0 = acc[ai][0][m][0], v1 = acc[ai][0][m][1]; const f32x4 c01 = rope[pos * 16 + (jj >> 1)], c23 = rope[pos * 16 + (jj >> 1) + 1];
;                     f32x4 w0, w1;
;                     w0[0] = v0[0] * c01[0] - v0[1] * c01[1]; w0[1] = v0[0] * c01[1] + v0[1] * c01[0];
;                     w0[2] = v0[2] * c01[2] - v0[3] * c01[3]; w0[3] = v0[2] * c01[3] + v0[3] * c01[2];
;                     w1[0] = v1[0] * c23[0] - v1[1] * c23[1]; w1[1] = v1[0] * c23[1] + v1[1] * c23[0];
;                     w1[2] = v1[2] * c23[2] - v1[3] * c23[3]; w1[3] = v1[2] * c23[3] + v1[3] * c23[2];
;                     *(u32x4*)(kr + (size_t)row * 64 + wc * 32 + 8 * fq) = pack8(w0, w1); }
.LBB0_1185:
	s_and_b32 s22, s96, 0x7ffffc00
	s_cmpk_lg_i32 s22, 0x800
	s_cbranch_scc0 .LBB0_1189
	s_and_b64 s[4:5], s[4:5], s[44:45]
	s_andn2_b64 vcc, exec, s[4:5]
	s_cbranch_vccnz .LBB0_1188
	v_add_u32_e32 v3, s69, v4
	v_ashrrev_i32_e32 v8, 2, v3
	v_lshlrev_b32_e32 v3, 4, v2
	v_and_b32_e32 v3, 0xfff0, v3
	v_add_u32_e32 v6, v3, v8
	v_ashrrev_i32_e32 v7, 31, v6
	v_lshl_add_u64 v[6:7], v[6:7], 4, s[38:39]
	v_mov_b32_e32 v250, v8
	v_mov_b32_e32 v251, v2
	v_lshlrev_b32_e32 v251, 4, v251
	v_and_b32_e32 v251, 0xfff0, v251
	v_add_lshl_u32 v251, v251, v250, 4
	global_load_dwordx4 v[182:185], v251, s[38:39]
	global_load_dwordx4 v[186:189], v251, s[38:39] offset:16
	v_add_u32_e32 v251, 16, v2
	v_lshlrev_b32_e32 v251, 4, v251
	v_and_b32_e32 v251, 0xfff0, v251
	v_add_lshl_u32 v251, v251, v250, 4
	global_load_dwordx4 v[190:193], v251, s[38:39]
	global_load_dwordx4 v[194:197], v251, s[38:39] offset:16
	v_add_u32_e32 v251, 32, v2
	v_lshlrev_b32_e32 v251, 4, v251
	v_and_b32_e32 v251, 0xfff0, v251
	v_add_lshl_u32 v251, v251, v250, 4
	global_load_dwordx4 v[234:237], v251, s[38:39]
	global_load_dwordx4 v[238:241], v251, s[38:39] offset:16
	v_add_u32_e32 v251, 48, v2
	v_lshlrev_b32_e32 v251, 4, v251
	v_and_b32_e32 v251, 0xfff0, v251
	v_add_lshl_u32 v251, v251, v250, 4
	global_load_dwordx4 v[242:245], v251, s[38:39]
	global_load_dwordx4 v[246:249], v251, s[38:39] offset:16
	v_ashrrev_i32_e32 v3, 31, v2
	v_add_u32_e32 v12, 16, v2
	v_lshlrev_b64 v[24:25], 7, v[2:3]
	v_lshlrev_b32_e32 v3, 4, v12
	v_ashrrev_i32_e32 v5, 31, v4
	v_and_b32_e32 v3, 0xfff0, v3
	v_lshlrev_b64 v[6:7], 1, v[4:5]
	v_lshl_add_u64 v[24:25], s[46:47], 0, v[24:25]
	v_add_u32_e32 v26, v3, v8
	v_lshl_add_u64 v[24:25], v[24:25], 0, v[6:7]
	v_ashrrev_i32_e32 v27, 31, v26
	v_lshl_add_u64 v[26:27], v[26:27], 4, s[38:39]
	s_waitcnt vmcnt(7)
	v_mov_b32_e32 v16, v182
	v_mov_b32_e32 v17, v183
	v_mov_b32_e32 v18, v184
	v_mov_b32_e32 v19, v185
	v_pk_mul_f32 v[28:29], v[160:161], v[18:19]
	v_pk_mul_f32 v[18:19], v[160:161], v[18:19] op_sel:[0,1] op_sel_hi:[1,0]
	s_waitcnt vmcnt(6)
	v_mov_b32_e32 v20, v186
	v_mov_b32_e32 v21, v187
	v_mov_b32_e32 v22, v188
	v_mov_b32_e32 v23, v189
	v_pk_mul_f32 v[32:33], v[156:157], v[22:23]
	v_pk_mul_f32 v[30:31], v[158:159], v[16:17]
	v_pk_mul_f32 v[16:17], v[158:159], v[16:17] op_sel:[0,1] op_sel_hi:[1,0]
	v_pk_mul_f32 v[178:179], v[154:155], v[20:21]
	v_pk_mul_f32 v[20:21], v[154:155], v[20:21] op_sel:[0,1] op_sel_hi:[1,0]
	v_pk_mul_f32 v[22:23], v[156:157], v[22:23] op_sel:[0,1] op_sel_hi:[1,0]
	v_add_f32_e32 v11, v18, v19
	v_sub_f32_e32 v19, v32, v33
	v_sub_f32_e32 v3, v30, v31
	v_add_f32_e32 v5, v16, v17
	v_sub_f32_e32 v9, v28, v29
	v_sub_f32_e32 v13, v178, v179
	v_add_f32_e32 v15, v20, v21
	v_add_f32_e32 v20, v22, v23
	v_cvt_pk_bf16_f32 v16, v3, v5
	v_cvt_pk_bf16_f32 v17, v9, v11
	v_cvt_pk_bf16_f32 v18, v13, v15
	v_cvt_pk_bf16_f32 v19, v19, v20
	global_store_dwordx4 v[24:25], v[16:19], off
	s_nop 1
	v_add_u32_e32 v251, 128, v2
	v_lshlrev_b32_e32 v251, 4, v251
	v_and_b32_e32 v251, 0xfff0, v251
	v_add_lshl_u32 v251, v251, v250, 4
	global_load_dwordx4 v[182:185], v251, s[38:39]
	global_load_dwordx4 v[186:189], v251, s[38:39] offset:16
	v_add_u32_e32 v24, 32, v2
	v_ashrrev_i32_e32 v13, 31, v12
	v_lshlrev_b32_e32 v3, 4, v24
	v_lshlrev_b64 v[12:13], 7, v[12:13]
	v_and_b32_e32 v3, 0xfff0, v3
	v_lshl_add_u64 v[12:13], s[46:47], 0, v[12:13]
	v_add_u32_e32 v26, v3, v8
	v_lshl_add_u64 v[12:13], v[12:13], 0, v[6:7]
	v_ashrrev_i32_e32 v27, 31, v26
	v_lshl_add_u64 v[26:27], v[26:27], 4, s[38:39]
	v_ashrrev_i32_e32 v25, 31, v24
	v_lshlrev_b64 v[24:25], 7, v[24:25]
	v_lshl_add_u64 v[24:25], s[46:47], 0, v[24:25]
	v_lshl_add_u64 v[24:25], v[24:25], 0, v[6:7]
	s_waitcnt vmcnt(8)
	v_mov_b32_e32 v16, v190
	v_mov_b32_e32 v17, v191
	v_mov_b32_e32 v18, v192
	v_mov_b32_e32 v19, v193
	v_pk_mul_f32 v[28:29], v[144:145], v[18:19]
	v_pk_mul_f32 v[18:19], v[144:145], v[18:19] op_sel:[0,1] op_sel_hi:[1,0]
	s_waitcnt vmcnt(7)
	v_mov_b32_e32 v20, v194
	v_mov_b32_e32 v21, v195
	v_mov_b32_e32 v22, v196
	v_mov_b32_e32 v23, v197
	v_pk_mul_f32 v[32:33], v[140:141], v[22:23]
	v_pk_mul_f32 v[178:179], v[138:139], v[20:21]
	v_pk_mul_f32 v[20:21], v[138:139], v[20:21] op_sel:[0,1] op_sel_hi:[1,0]
	v_pk_mul_f32 v[30:31], v[142:143], v[16:17]
	v_pk_mul_f32 v[16:17], v[142:143], v[16:17] op_sel:[0,1] op_sel_hi:[1,0]
	v_pk_mul_f32 v[22:23], v[140:141], v[22:23] op_sel:[0,1] op_sel_hi:[1,0]
	v_add_f32_e32 v11, v18, v19
	v_add_f32_e32 v18, v20, v21
	v_sub_f32_e32 v19, v32, v33
	v_sub_f32_e32 v3, v30, v31
	v_add_f32_e32 v5, v16, v17
	v_sub_f32_e32 v9, v28, v29
	v_sub_f32_e32 v15, v178, v179
	v_add_f32_e32 v20, v22, v23
	v_cvt_pk_bf16_f32 v16, v3, v5
	v_cvt_pk_bf16_f32 v17, v9, v11
	v_cvt_pk_bf16_f32 v18, v15, v18
	v_cvt_pk_bf16_f32 v19, v19, v20
	global_store_dwordx4 v[12:13], v[16:19], off
	s_nop 1
	v_add_u32_e32 v251, 144, v2
	v_lshlrev_b32_e32 v251, 4, v251
	v_and_b32_e32 v251, 0xfff0, v251
	v_add_lshl_u32 v251, v251, v250, 4
	global_load_dwordx4 v[190:193], v251, s[38:39]
	global_load_dwordx4 v[194:197], v251, s[38:39] offset:16
	v_add_u32_e32 v12, 48, v2
	v_lshlrev_b32_e32 v3, 4, v12
	v_and_b32_e32 v3, 0xfff0, v3
	v_add_u32_e32 v26, v3, v8
	v_ashrrev_i32_e32 v27, 31, v26
	v_lshl_add_u64 v[26:27], v[26:27], 4, s[38:39]
	s_waitcnt vmcnt(9)
	v_mov_b32_e32 v16, v234
	v_mov_b32_e32 v17, v235
	v_mov_b32_e32 v18, v236
	v_mov_b32_e32 v19, v237
	v_pk_mul_f32 v[28:29], v[132:133], v[18:19]
	v_pk_mul_f32 v[18:19], v[132:133], v[18:19] op_sel:[0,1] op_sel_hi:[1,0]
	s_waitcnt vmcnt(8)
; __device__ __forceinline__ u32x4 pack8(f32x4 a, f32x4 b) { u32x4 w; w.x = cvtpk(a[0], a[1]); w.y = cvtpk(a[2], a[3]); w.z = cvtpk(b[0], b[1]); w.w = cvtpk(b[2], b[3]); return w; }
;     __device__ __forceinline__ void operator()(const Acc& acc, const Unit& u, int wr, int wc, int fr, int fq) const {
;     ...
;         } else if (u.col0 == 8192 && wc < 2) {
; #pragma unroll
;             for (int ai = 0; ai < 2; ++ai)
; #pragma unroll
;                 for (int m = 0; m < 4; ++m) { const int row = row0 + ai * HALF + m * 16, pos = row & (SEQ - 1); const int jj = (wc * 32 + 8 * fq) >> 1;
;                     const f32x4 v0 = acc[ai][0][m][0], v1 = acc[ai][0][m][1]; const f32x4 c01 = rope[pos * 16 + (jj >> 1)], c23 = rope[pos * 16 + (jj >> 1) + 1];
;                     f32x4 w0, w1;
;                     w0[0] = v0[0] * c01[0] - v0[1] * c01[1]; w0[1] = v0[0] * c01[1] + v0[1] * c01[0];
;                     w0[2] = v0[2] * c01[2] - v0[3] * c01[3]; w0[3] = v0[2] * c01[3] + v0[3] * c01[2];
;                     w1[0] = v1[0] * c23[0] - v1[1] * c23[1]; w1[1] = v1[0] * c23[1] + v1[1] * c23[0];
;                     w1[2] = v1[2] * c23[2] - v1[3] * c23[3]; w1[3] = v1[2] * c23[3] + v1[3] * c23[2];
;                     *(u32x4*)(kr + (size_t)row * 64 + wc * 32 + 8 * fq) = pack8(w0, w1); }
	v_mov_b32_e32 v20, v238
	v_mov_b32_e32 v21, v239
	v_mov_b32_e32 v22, v240
	v_mov_b32_e32 v23, v241
	v_pk_mul_f32 v[32:33], v[124:125], v[22:23]
	v_pk_mul_f32 v[30:31], v[130:131], v[16:17]
	v_pk_mul_f32 v[16:17], v[130:131], v[16:17] op_sel:[0,1] op_sel_hi:[1,0]
	v_pk_mul_f32 v[178:179], v[122:123], v[20:21]
	v_pk_mul_f32 v[20:21], v[122:123], v[20:21] op_sel:[0,1] op_sel_hi:[1,0]
	v_pk_mul_f32 v[22:23], v[124:125], v[22:23] op_sel:[0,1] op_sel_hi:[1,0]
	v_add_f32_e32 v11, v18, v19
	v_sub_f32_e32 v19, v32, v33
	v_sub_f32_e32 v3, v30, v31
	v_add_f32_e32 v5, v16, v17
	v_sub_f32_e32 v9, v28, v29
	v_sub_f32_e32 v13, v178, v179
	v_add_f32_e32 v15, v20, v21
	v_add_f32_e32 v20, v22, v23
	v_cvt_pk_bf16_f32 v16, v3, v5
	v_cvt_pk_bf16_f32 v17, v9, v11
	v_cvt_pk_bf16_f32 v18, v13, v15
	v_cvt_pk_bf16_f32 v19, v19, v20
	global_store_dwordx4 v[24:25], v[16:19], off
	s_nop 1
	v_add_u32_e32 v251, 160, v2
	v_lshlrev_b32_e32 v251, 4, v251
	v_and_b32_e32 v251, 0xfff0, v251
	v_add_lshl_u32 v251, v251, v250, 4
	global_load_dwordx4 v[234:237], v251, s[38:39]
	global_load_dwordx4 v[238:241], v251, s[38:39] offset:16
	v_add_u32_e32 v24, 0x80, v2
	v_ashrrev_i32_e32 v13, 31, v12
	v_lshlrev_b32_e32 v3, 4, v24
	v_lshlrev_b64 v[12:13], 7, v[12:13]
	v_and_b32_e32 v3, 0xfff0, v3
	v_lshl_add_u64 v[12:13], s[46:47], 0, v[12:13]
	v_add_u32_e32 v26, v3, v8
	v_lshl_add_u64 v[12:13], v[12:13], 0, v[6:7]
	v_ashrrev_i32_e32 v27, 31, v26
	v_lshl_add_u64 v[26:27], v[26:27], 4, s[38:39]
	v_ashrrev_i32_e32 v25, 31, v24
	v_lshlrev_b64 v[24:25], 7, v[24:25]
	v_lshl_add_u64 v[24:25], s[46:47], 0, v[24:25]
	v_lshl_add_u64 v[24:25], v[24:25], 0, v[6:7]
	s_waitcnt vmcnt(10)
	v_mov_b32_e32 v16, v242
	v_mov_b32_e32 v17, v243
	v_mov_b32_e32 v18, v244
	v_mov_b32_e32 v19, v245
	v_pk_mul_f32 v[28:29], v[116:117], v[18:19]
	v_pk_mul_f32 v[18:19], v[116:117], v[18:19] op_sel:[0,1] op_sel_hi:[1,0]
	s_waitcnt vmcnt(9)
	v_mov_b32_e32 v20, v246
	v_mov_b32_e32 v21, v247
	v_mov_b32_e32 v22, v248
	v_mov_b32_e32 v23, v249
	v_pk_mul_f32 v[32:33], v[108:109], v[22:23]
	v_pk_mul_f32 v[178:179], v[106:107], v[20:21]
	v_pk_mul_f32 v[20:21], v[106:107], v[20:21] op_sel:[0,1] op_sel_hi:[1,0]
	v_pk_mul_f32 v[30:31], v[114:115], v[16:17]
	v_pk_mul_f32 v[16:17], v[114:115], v[16:17] op_sel:[0,1] op_sel_hi:[1,0]
	v_pk_mul_f32 v[22:23], v[108:109], v[22:23] op_sel:[0,1] op_sel_hi:[1,0]
	v_add_f32_e32 v11, v18, v19
	v_add_f32_e32 v18, v20, v21
	v_sub_f32_e32 v19, v32, v33
	v_sub_f32_e32 v3, v30, v31
	v_add_f32_e32 v5, v16, v17
	v_sub_f32_e32 v9, v28, v29
	v_sub_f32_e32 v15, v178, v179
	v_add_f32_e32 v20, v22, v23
	v_cvt_pk_bf16_f32 v16, v3, v5
	v_cvt_pk_bf16_f32 v17, v9, v11
	v_cvt_pk_bf16_f32 v18, v15, v18
	v_cvt_pk_bf16_f32 v19, v19, v20
	global_store_dwordx4 v[12:13], v[16:19], off
	s_nop 1
	v_add_u32_e32 v251, 176, v2
	v_lshlrev_b32_e32 v251, 4, v251
	v_and_b32_e32 v251, 0xfff0, v251
	v_add_lshl_u32 v251, v251, v250, 4
	global_load_dwordx4 v[242:245], v251, s[38:39]
	global_load_dwordx4 v[246:249], v251, s[38:39] offset:16
	v_add_u32_e32 v12, 0x90, v2
	v_lshlrev_b32_e32 v3, 4, v12
	v_and_b32_e32 v3, 0xfff0, v3
	v_add_u32_e32 v26, v3, v8
	v_ashrrev_i32_e32 v27, 31, v26
	v_lshl_add_u64 v[26:27], v[26:27], 4, s[38:39]
	s_waitcnt vmcnt(10)
	v_mov_b32_e32 v16, v182
	v_mov_b32_e32 v17, v183
	v_mov_b32_e32 v18, v184
	v_mov_b32_e32 v19, v185
	v_pk_mul_f32 v[28:29], v[96:97], v[18:19]
	v_pk_mul_f32 v[18:19], v[96:97], v[18:19] op_sel:[0,1] op_sel_hi:[1,0]
	s_waitcnt vmcnt(9)
	v_mov_b32_e32 v20, v186
	v_mov_b32_e32 v21, v187
	v_mov_b32_e32 v22, v188
	v_mov_b32_e32 v23, v189
	v_pk_mul_f32 v[32:33], v[92:93], v[22:23]
	v_pk_mul_f32 v[30:31], v[94:95], v[16:17]
	v_pk_mul_f32 v[16:17], v[94:95], v[16:17] op_sel:[0,1] op_sel_hi:[1,0]
	v_pk_mul_f32 v[178:179], v[90:91], v[20:21]
	v_pk_mul_f32 v[20:21], v[90:91], v[20:21] op_sel:[0,1] op_sel_hi:[1,0]
	v_pk_mul_f32 v[22:23], v[92:93], v[22:23] op_sel:[0,1] op_sel_hi:[1,0]
	v_add_f32_e32 v11, v18, v19
	v_sub_f32_e32 v19, v32, v33
	v_sub_f32_e32 v3, v30, v31
	v_add_f32_e32 v5, v16, v17
	v_sub_f32_e32 v9, v28, v29
	v_sub_f32_e32 v13, v178, v179
	v_add_f32_e32 v15, v20, v21
	v_add_f32_e32 v20, v22, v23
	v_cvt_pk_bf16_f32 v16, v3, v5
	v_cvt_pk_bf16_f32 v17, v9, v11
	v_cvt_pk_bf16_f32 v18, v13, v15
	v_cvt_pk_bf16_f32 v19, v19, v20
	global_store_dwordx4 v[24:25], v[16:19], off
	s_nop 1
	v_add_u32_e32 v24, 0xa0, v2
	v_ashrrev_i32_e32 v13, 31, v12
	v_lshlrev_b32_e32 v3, 4, v24
	v_lshlrev_b64 v[12:13], 7, v[12:13]
	v_and_b32_e32 v3, 0xfff0, v3
	v_lshl_add_u64 v[12:13], s[46:47], 0, v[12:13]
	v_add_u32_e32 v26, v3, v8
	v_lshl_add_u64 v[12:13], v[12:13], 0, v[6:7]
	v_ashrrev_i32_e32 v27, 31, v26
	v_lshl_add_u64 v[26:27], v[26:27], 4, s[38:39]
	v_ashrrev_i32_e32 v25, 31, v24
	v_lshlrev_b64 v[24:25], 7, v[24:25]
	v_lshl_add_u64 v[24:25], s[46:47], 0, v[24:25]
	v_lshl_add_u64 v[24:25], v[24:25], 0, v[6:7]
	s_waitcnt vmcnt(8)
; __device__ __forceinline__ u32x4 pack8(f32x4 a, f32x4 b) { u32x4 w; w.x = cvtpk(a[0], a[1]); w.y = cvtpk(a[2], a[3]); w.z = cvtpk(b[0], b[1]); w.w = cvtpk(b[2], b[3]); return w; }
;     __device__ __forceinline__ void operator()(const Acc& acc, const Unit& u, int wr, int wc, int fr, int fq) const {
;     ...
;         } else if (u.col0 == 8192 && wc < 2) {
; #pragma unroll
;             for (int ai = 0; ai < 2; ++ai)
; #pragma unroll
;                 for (int m = 0; m < 4; ++m) { const int row = row0 + ai * HALF + m * 16, pos = row & (SEQ - 1); const int jj = (wc * 32 + 8 * fq) >> 1;
;                     const f32x4 v0 = acc[ai][0][m][0], v1 = acc[ai][0][m][1]; const f32x4 c01 = rope[pos * 16 + (jj >> 1)], c23 = rope[pos * 16 + (jj >> 1) + 1];
;                     f32x4 w0, w1;
;                     w0[0] = v0[0] * c01[0] - v0[1] * c01[1]; w0[1] = v0[0] * c01[1] + v0[1] * c01[0];
;                     w0[2] = v0[2] * c01[2] - v0[3] * c01[3]; w0[3] = v0[2] * c01[3] + v0[3] * c01[2];
;                     w1[0] = v1[0] * c23[0] - v1[1] * c23[1]; w1[1] = v1[0] * c23[1] + v1[1] * c23[0];
;                     w1[2] = v1[2] * c23[2] - v1[3] * c23[3]; w1[3] = v1[2] * c23[3] + v1[3] * c23[2];
;                     *(u32x4*)(kr + (size_t)row * 64 + wc * 32 + 8 * fq) = pack8(w0, w1); }
	v_mov_b32_e32 v16, v190
	v_mov_b32_e32 v17, v191
	v_mov_b32_e32 v18, v192
	v_mov_b32_e32 v19, v193
	v_pk_mul_f32 v[28:29], v[72:73], v[18:19]
	v_pk_mul_f32 v[18:19], v[72:73], v[18:19] op_sel:[0,1] op_sel_hi:[1,0]
	s_waitcnt vmcnt(7)
	v_mov_b32_e32 v20, v194
	v_mov_b32_e32 v21, v195
	v_mov_b32_e32 v22, v196
	v_mov_b32_e32 v23, v197
	v_pk_mul_f32 v[32:33], v[68:69], v[22:23]
	v_pk_mul_f32 v[178:179], v[66:67], v[20:21]
	v_pk_mul_f32 v[20:21], v[66:67], v[20:21] op_sel:[0,1] op_sel_hi:[1,0]
	v_pk_mul_f32 v[30:31], v[70:71], v[16:17]
	v_pk_mul_f32 v[16:17], v[70:71], v[16:17] op_sel:[0,1] op_sel_hi:[1,0]
	v_pk_mul_f32 v[22:23], v[68:69], v[22:23] op_sel:[0,1] op_sel_hi:[1,0]
	v_add_f32_e32 v11, v18, v19
	v_add_f32_e32 v18, v20, v21
	v_sub_f32_e32 v19, v32, v33
	v_sub_f32_e32 v3, v30, v31
	v_add_f32_e32 v5, v16, v17
	v_sub_f32_e32 v9, v28, v29
	v_sub_f32_e32 v15, v178, v179
	v_add_f32_e32 v20, v22, v23
	v_cvt_pk_bf16_f32 v16, v3, v5
	v_cvt_pk_bf16_f32 v17, v9, v11
	v_cvt_pk_bf16_f32 v18, v15, v18
	v_cvt_pk_bf16_f32 v19, v19, v20
	global_store_dwordx4 v[12:13], v[16:19], off
	s_nop 1
	v_add_u32_e32 v12, 0xb0, v2
	v_lshlrev_b32_e32 v3, 4, v12
	v_and_b32_e32 v3, 0xfff0, v3
	v_add_u32_e32 v8, v3, v8
	v_ashrrev_i32_e32 v9, 31, v8
	v_lshl_add_u64 v[8:9], v[8:9], 4, s[38:39]
	s_waitcnt vmcnt(6)
	v_mov_b32_e32 v16, v234
	v_mov_b32_e32 v17, v235
	v_mov_b32_e32 v18, v236
	v_mov_b32_e32 v19, v237
	v_pk_mul_f32 v[26:27], v[52:53], v[18:19]
	v_pk_mul_f32 v[18:19], v[52:53], v[18:19] op_sel:[0,1] op_sel_hi:[1,0]
	s_waitcnt vmcnt(5)
	v_mov_b32_e32 v20, v238
	v_mov_b32_e32 v21, v239
	v_mov_b32_e32 v22, v240
	v_mov_b32_e32 v23, v241
	v_pk_mul_f32 v[30:31], v[44:45], v[22:23]
	v_pk_mul_f32 v[32:33], v[42:43], v[20:21]
	v_pk_mul_f32 v[20:21], v[42:43], v[20:21] op_sel:[0,1] op_sel_hi:[1,0]
	v_pk_mul_f32 v[28:29], v[50:51], v[16:17]
	v_pk_mul_f32 v[16:17], v[50:51], v[16:17] op_sel:[0,1] op_sel_hi:[1,0]
	v_pk_mul_f32 v[22:23], v[44:45], v[22:23] op_sel:[0,1] op_sel_hi:[1,0]
	v_add_f32_e32 v13, v18, v19
	v_add_f32_e32 v18, v20, v21
	v_sub_f32_e32 v19, v30, v31
	v_sub_f32_e32 v3, v28, v29
	v_add_f32_e32 v5, v16, v17
	v_sub_f32_e32 v11, v26, v27
	v_sub_f32_e32 v15, v32, v33
	v_add_f32_e32 v20, v22, v23
	v_cvt_pk_bf16_f32 v16, v3, v5
	v_cvt_pk_bf16_f32 v17, v11, v13
	v_cvt_pk_bf16_f32 v18, v15, v18
	v_cvt_pk_bf16_f32 v19, v19, v20
	global_store_dwordx4 v[24:25], v[16:19], off
	s_nop 1
	v_ashrrev_i32_e32 v13, 31, v12
	v_lshlrev_b64 v[8:9], 7, v[12:13]
	v_lshl_add_u64 v[8:9], s[46:47], 0, v[8:9]
	v_lshl_add_u64 v[6:7], v[8:9], 0, v[6:7]
	s_waitcnt vmcnt(4)
	v_mov_b32_e32 v16, v242
	v_mov_b32_e32 v17, v243
	v_mov_b32_e32 v18, v244
	v_mov_b32_e32 v19, v245
	v_pk_mul_f32 v[12:13], v[40:41], v[18:19]
	v_pk_mul_f32 v[18:19], v[40:41], v[18:19] op_sel:[0,1] op_sel_hi:[1,0]
	s_waitcnt vmcnt(3)
	v_mov_b32_e32 v20, v246
	v_mov_b32_e32 v21, v247
	v_mov_b32_e32 v22, v248
	v_mov_b32_e32 v23, v249
	v_pk_mul_f32 v[26:27], v[36:37], v[22:23]
	v_pk_mul_f32 v[24:25], v[38:39], v[16:17]
	v_pk_mul_f32 v[16:17], v[38:39], v[16:17] op_sel:[0,1] op_sel_hi:[1,0]
	v_pk_mul_f32 v[28:29], v[34:35], v[20:21]
	v_pk_mul_f32 v[20:21], v[34:35], v[20:21] op_sel:[0,1] op_sel_hi:[1,0]
	v_pk_mul_f32 v[22:23], v[36:37], v[22:23] op_sel:[0,1] op_sel_hi:[1,0]
	v_sub_f32_e32 v11, v12, v13
	v_add_f32_e32 v12, v18, v19
	v_sub_f32_e32 v19, v26, v27
	v_sub_f32_e32 v3, v24, v25
	v_add_f32_e32 v5, v16, v17
	v_sub_f32_e32 v13, v28, v29
	v_add_f32_e32 v15, v20, v21
	v_add_f32_e32 v20, v22, v23
	v_cvt_pk_bf16_f32 v16, v3, v5
	v_cvt_pk_bf16_f32 v17, v11, v12
	v_cvt_pk_bf16_f32 v18, v13, v15
	v_cvt_pk_bf16_f32 v19, v19, v20
	global_store_dwordx4 v[6:7], v[16:19], off
	s_nop 1

; __device__ __forceinline__ u32x4 pack8(f32x4 a, f32x4 b) { u32x4 w; w.x = cvtpk(a[0], a[1]); w.y = cvtpk(a[2], a[3]); w.z = cvtpk(b[0], b[1]); w.w = cvtpk(b[2], b[3]); return w; }
; __device__ __forceinline__ float latent_rstd(const float* ssp, int row, int which) {
;     const f32x4 a = *(const f32x4*)(ssp + ((size_t)row * 2 + which) * 8), b = *(const f32x4*)(ssp + ((size_t)row * 2 + which) * 8 + 4);
;     return 1.0f / sqrtf((((a[0] + a[1]) + (a[2] + a[3])) + ((b[0] + b[1]) + (b[2] + b[3]))) * (1.0f / 512.0f) + 1e-6f);
; }
;     __device__ __forceinline__ void operator()(const Acc& acc, const Unit& u, int wr, int wc, int fr, int fq) const {
;         const int row0 = u.row0 + wr * 64 + fr, col0 = u.col0 + wc * 32 + 8 * fq;
; #pragma unroll
;         for (int ai = 0; ai < 2; ++ai)
; #pragma unroll
;             for (int m = 0; m < 4; ++m) { const int row = row0 + ai * HALF + m * 16, pos = row & (SEQ - 1); const float rs = latent_rstd(ssp, row, 0); bf16_t* rowp = O + (size_t)row * ldc + col0;
; #pragma unroll
;                 for (int bj = 0; bj < 2; ++bj) { f32x4 v0 = acc[ai][bj][m][0] * rs, v1 = acc[ai][bj][m][1] * rs; const int d = (col0 + bj * HALF) % 192;
;                     if (d >= 128) { const int jj = (d - 128) >> 1; const f32x4 c01 = rope[pos * 16 + (jj >> 1)], c23 = rope[pos * 16 + (jj >> 1) + 1];
;                         f32x4 w0, w1;
;                         w0[0] = v0[0] * c01[0] - v0[1] * c01[1]; w0[1] = v0[0] * c01[1] + v0[1] * c01[0];
;                         w0[2] = v0[2] * c01[2] - v0[3] * c01[3]; w0[3] = v0[2] * c01[3] + v0[3] * c01[2];
;                         w1[0] = v1[0] * c23[0] - v1[1] * c23[1]; w1[1] = v1[0] * c23[1] + v1[1] * c23[0];
;                         w1[2] = v1[2] * c23[2] - v1[3] * c23[3]; w1[3] = v1[2] * c23[3] + v1[3] * c23[2];
;                         v0 = w0; v1 = w1; }
;                     *(u32x4*)(rowp + bj * HALF) = pack8(v0, v1); } }
.LBB0_1265:
	v_mbcnt_lo_u32_b32 v130, -1, 0
	v_mbcnt_hi_u32_b32 v130, -1, v130
	s_add_i32 s4, s26, s65
	v_and_b32_e32 v132, 15, v130
	v_add_u32_e32 v134, s4, v132
	v_ashrrev_i32_e32 v135, 31, v134
	v_lshlrev_b64 v[132:133], 6, v[134:135]
	v_lshl_add_u64 v[132:133], s[10:11], 0, v[132:133]
	v_lshlrev_b32_e32 v250, 6, v134
	global_load_dwordx4 v[182:185], v250, s[10:11]
	global_load_dwordx4 v[186:189], v250, s[10:11] offset:16
	v_add_u32_e32 v250, 16, v134
	v_lshlrev_b32_e32 v250, 6, v250
	global_load_dwordx4 v[190:193], v250, s[10:11]
	global_load_dwordx4 v[194:197], v250, s[10:11] offset:16
	v_add_u32_e32 v250, 32, v134
	v_lshlrev_b32_e32 v250, 6, v250
	global_load_dwordx4 v[200:203], v250, s[10:11]
	global_load_dwordx4 v[204:207], v250, s[10:11] offset:16
	v_add_u32_e32 v250, 48, v134
	v_lshlrev_b32_e32 v250, 6, v250
	global_load_dwordx4 v[208:211], v250, s[10:11]
	global_load_dwordx4 v[212:215], v250, s[10:11] offset:16
	v_ashrrev_i32_e32 v130, 1, v130
	s_add_i32 s3, s3, s66
	v_and_b32_e32 v130, -8, v130
	v_add_u32_e32 v132, s3, v130
	v_lshlrev_b32_e32 v130, 4, v134
	v_and_b32_e32 v157, 0xfff0, v130
	v_mul_hi_i32 v130, v132, s88
	v_lshrrev_b32_e32 v133, 31, v130
	v_lshrrev_b32_e32 v130, 5, v130
	v_add_u32_e32 v130, v130, v133
	v_mul_lo_u32 v130, v130, s90
	v_sub_u32_e32 v130, v132, v130
	v_cmp_lt_i32_e64 s[4:5], s91, v130
	v_add_u32_e32 v130, 0xffffff80, v130
	v_add_u32_e32 v251, 0x80, v132
	v_mul_hi_i32 v253, v251, s88
	v_lshrrev_b32_e32 v254, 31, v253
	v_lshrrev_b32_e32 v253, 5, v253
	v_add_u32_e32 v253, v253, v254
	v_mul_lo_u32 v253, v253, s90
	v_sub_u32_e32 v251, v251, v253
	v_add_u32_e32 v251, 0xffffff80, v251
	v_max_i32_e32 v251, 0, v251
	v_lshrrev_b32_e32 v251, 2, v251
	v_lshrrev_b32_e32 v253, 2, v130
	v_cndmask_b32_e64 v255, v251, v253, s[4:5]
	v_mov_b32_e32 v251, v134
	v_lshlrev_b32_e32 v251, 4, v251
	v_and_b32_e32 v251, 0xfff0, v251
	v_add_lshl_u32 v251, v251, v255, 4
	global_load_dwordx4 v[216:219], v251, s[38:39]
	global_load_dwordx4 v[220:223], v251, s[38:39] offset:16
	v_add_u32_e32 v251, 16, v134
	v_lshlrev_b32_e32 v251, 4, v251
	v_and_b32_e32 v251, 0xfff0, v251
	v_add_lshl_u32 v251, v251, v255, 4
	global_load_dwordx4 v[224:227], v251, s[38:39]
	global_load_dwordx4 v[228:231], v251, s[38:39] offset:16
	v_add_u32_e32 v251, 32, v134
	v_lshlrev_b32_e32 v251, 4, v251
	v_and_b32_e32 v251, 0xfff0, v251
	v_add_lshl_u32 v251, v251, v255, 4
	global_load_dwordx4 v[232:235], v251, s[38:39]
	global_load_dwordx4 v[236:239], v251, s[38:39] offset:16
	v_add_u32_e32 v251, 48, v134
	v_lshlrev_b32_e32 v251, 4, v251
	v_and_b32_e32 v251, 0xfff0, v251
	v_add_lshl_u32 v251, v251, v255, 4
	global_load_dwordx4 v[240:243], v251, s[38:39]
	global_load_dwordx4 v[244:247], v251, s[38:39] offset:16
	s_waitcnt vmcnt(14)
	v_mov_b32_e32 v136, v182
	v_mov_b32_e32 v137, v183
	v_mov_b32_e32 v138, v184
	v_mov_b32_e32 v139, v185
	v_mov_b32_e32 v162, v136
	v_mov_b32_e32 v158, v186
	v_mov_b32_e32 v159, v187
	v_mov_b32_e32 v160, v188
	v_mov_b32_e32 v161, v189
	v_mov_b32_e32 v163, v158
	v_mov_b32_e32 v158, v137
	v_mov_b32_e32 v136, v138
	v_mov_b32_e32 v137, v160
	v_mov_b32_e32 v160, v139
	v_pk_add_f32 v[138:139], v[162:163], v[158:159]
	v_pk_add_f32 v[136:137], v[136:137], v[160:161]
	s_nop 0
	v_pk_add_f32 v[136:137], v[138:139], v[136:137]
	s_nop 0
	v_add_f32_e32 v133, v136, v137
	v_fmamk_f32 v133, v133, 0x3b000000, v155
	v_mul_f32_e32 v135, 0x4f800000, v133
	v_cmp_gt_f32_e32 vcc, s89, v133
	s_nop 1
	v_cndmask_b32_e32 v133, v133, v135, vcc
	v_sqrt_f32_e32 v135, v133
	s_nop 0
	v_add_u32_e32 v136, -1, v135
	v_add_u32_e32 v137, 1, v135
	v_fma_f32 v138, -v136, v135, v133
	v_fma_f32 v139, -v137, v135, v133
	v_cmp_ge_f32_e64 s[6:7], 0, v138
	s_nop 1
	v_cndmask_b32_e64 v135, v135, v136, s[6:7]
	v_cmp_lt_f32_e64 s[6:7], 0, v139
	s_nop 1
	v_cndmask_b32_e64 v135, v135, v137, s[6:7]
	v_mul_f32_e32 v136, 0x37800000, v135
	v_cndmask_b32_e32 v135, v135, v136, vcc
	v_cmp_class_f32_e32 vcc, v133, v156
	s_nop 1
	v_cndmask_b32_e32 v133, v135, v133, vcc
	v_div_scale_f32 v135, s[6:7], v133, v133, 1.0
	v_rcp_f32_e32 v136, v135
	v_div_scale_f32 v137, vcc, 1.0, v133, 1.0
	v_fma_f32 v138, -v135, v136, 1.0
	v_fmac_f32_e32 v136, v138, v136
	v_mul_f32_e32 v138, v137, v136
	v_fma_f32 v139, -v135, v138, v137
	v_fmac_f32_e32 v138, v139, v136
	v_fma_f32 v135, -v135, v138, v137
	v_div_fmas_f32 v135, v135, v136, v138
	v_div_fixup_f32 v136, v135, v133, 1.0
	v_pk_mul_f32 v[138:139], v[128:129], v[136:137] op_sel_hi:[1,0]
	v_pk_mul_f32 v[126:127], v[126:127], v[136:137] op_sel_hi:[1,0]
	v_pk_mul_f32 v[128:129], v[124:125], v[136:137] op_sel_hi:[1,0]
	v_pk_mul_f32 v[124:125], v[122:123], v[136:137] op_sel_hi:[1,0]
	v_lshrrev_b32_e32 v135, 2, v130
	s_and_saveexec_b64 s[6:7], s[4:5]
	s_cbranch_execz .LBB0_1267
	v_add_u32_e32 v130, v135, v157
	v_lshl_add_u64 v[122:123], v[130:131], 4, s[38:39]
	s_waitcnt vmcnt(7)
	v_mov_b32_e32 v158, v216
	v_mov_b32_e32 v159, v217
	v_mov_b32_e32 v160, v218
	v_mov_b32_e32 v161, v219
	v_pk_mul_f32 v[162:163], v[126:127], v[158:159] op_sel:[1,1] op_sel_hi:[1,0]
	v_mul_f32_e32 v130, v139, v161
	v_mul_f32_e32 v172, v139, v160
	s_waitcnt vmcnt(6)
	v_mov_b32_e32 v168, v220
	v_mov_b32_e32 v169, v221
	v_mov_b32_e32 v170, v222
	v_mov_b32_e32 v171, v223
	v_pk_mul_f32 v[176:177], v[124:125], v[168:169] op_sel:[1,1] op_sel_hi:[1,0]
	v_mul_f32_e32 v178, v129, v171
	v_mul_f32_e32 v180, v129, v170
	v_pk_mul_f32 v[122:123], v[126:127], v[158:159]
	v_pk_mul_f32 v[174:175], v[124:125], v[168:169]
	v_pk_fma_f32 v[126:127], v[126:127], v[158:159], v[162:163] op_sel_hi:[0,1,1]
	v_pk_fma_f32 v[158:159], v[138:139], v[160:161], v[130:131] op_sel_hi:[1,1,0] neg_lo:[0,0,1] neg_hi:[0,0,1]
	v_pk_fma_f32 v[160:161], v[138:139], v[160:161], v[172:173] op_sel:[0,1,0] op_sel_hi:[1,0,0]
	v_pk_fma_f32 v[124:125], v[124:125], v[168:169], v[176:177] op_sel_hi:[0,1,1]
	v_pk_fma_f32 v[168:169], v[128:129], v[170:171], v[178:179] op_sel_hi:[1,1,0] neg_lo:[0,0,1] neg_hi:[0,0,1]
	v_pk_fma_f32 v[170:171], v[128:129], v[170:171], v[180:181] op_sel:[0,1,0] op_sel_hi:[1,0,0]
	v_sub_f32_e32 v126, v122, v162
	v_sub_f32_e32 v124, v174, v176
	v_mov_b32_e32 v138, v158
	v_mov_b32_e32 v139, v160
	v_mov_b32_e32 v128, v168
	v_mov_b32_e32 v129, v170
; __device__ __forceinline__ u32x4 pack8(f32x4 a, f32x4 b) { u32x4 w; w.x = cvtpk(a[0], a[1]); w.y = cvtpk(a[2], a[3]); w.z = cvtpk(b[0], b[1]); w.w = cvtpk(b[2], b[3]); return w; }
;     __device__ __forceinline__ void operator()(const Acc& acc, const Unit& u, int wr, int wc, int fr, int fq) const {
;     ...
;             for (int m = 0; m < 4; ++m) { const int row = row0 + ai * HALF + m * 16, pos = row & (SEQ - 1); const float rs = latent_rstd(ssp, row, 0); bf16_t* rowp = O + (size_t)row * ldc + col0;
; #pragma unroll
;                 for (int bj = 0; bj < 2; ++bj) { f32x4 v0 = acc[ai][bj][m][0] * rs, v1 = acc[ai][bj][m][1] * rs; const int d = (col0 + bj * HALF) % 192;
;                     if (d >= 128) { const int jj = (d - 128) >> 1; const f32x4 c01 = rope[pos * 16 + (jj >> 1)], c23 = rope[pos * 16 + (jj >> 1) + 1];
;                         f32x4 w0, w1;
;                         w0[0] = v0[0] * c01[0] - v0[1] * c01[1]; w0[1] = v0[0] * c01[1] + v0[1] * c01[0];
;                         w0[2] = v0[2] * c01[2] - v0[3] * c01[3]; w0[3] = v0[2] * c01[3] + v0[3] * c01[2];
;                         w1[0] = v1[0] * c23[0] - v1[1] * c23[1]; w1[1] = v1[0] * c23[1] + v1[1] * c23[0];
;                         w1[2] = v1[2] * c23[2] - v1[3] * c23[3]; w1[3] = v1[2] * c23[3] + v1[3] * c23[2];
;                         v0 = w0; v1 = w1; }
;                     *(u32x4*)(rowp + bj * HALF) = pack8(v0, v1); } }
.LBB0_1267:
	s_or_b64 exec, exec, s[6:7]
	v_cvt_pk_bf16_f32 v158, v126, v127
	v_cvt_pk_bf16_f32 v159, v138, v139
	v_cvt_pk_bf16_f32 v160, v124, v125
	v_mov_b32_e32 v124, v136
	v_mov_b32_e32 v125, v136
	v_pk_mul_f32 v[120:121], v[120:121], v[124:125]
	v_pk_mul_f32 v[116:117], v[116:117], v[124:125]
	v_add_u32_e32 v124, 0x80, v132
	v_mul_hi_i32 v125, v124, s88
	v_lshrrev_b32_e32 v126, 31, v125
	v_lshrrev_b32_e32 v125, 5, v125
	v_add_u32_e32 v125, v125, v126
	v_mov_b64_e32 v[122:123], s[30:31]
	v_mul_lo_u32 v125, v125, s90
	v_mad_i64_i32 v[122:123], s[6:7], v134, s92, v[122:123]
	v_sub_u32_e32 v124, v124, v125
	v_mov_b32_e32 v137, v136
	v_ashrrev_i32_e32 v133, 31, v132
	v_cmp_lt_i32_e64 s[6:7], s91, v124
	v_add_u32_e32 v124, 0xffffff80, v124
	v_lshl_add_u64 v[122:123], v[132:133], 1, v[122:123]
	v_pk_mul_f32 v[118:119], v[118:119], v[136:137]
	v_pk_mul_f32 v[114:115], v[114:115], v[136:137]
	v_lshrrev_b32_e32 v124, 2, v124
	v_cvt_pk_bf16_f32 v161, v128, v129
	global_store_dwordx4 v[122:123], v[158:161], off
	s_and_saveexec_b64 s[8:9], s[6:7]
	s_cbranch_execz .LBB0_1269
	v_add_u32_e32 v130, v124, v157
	v_lshl_add_u64 v[136:137], v[130:131], 4, s[38:39]
	s_waitcnt vmcnt(8)
	v_mov_b32_e32 v126, v216
	v_mov_b32_e32 v127, v217
	v_mov_b32_e32 v128, v218
	v_mov_b32_e32 v129, v219
	v_pk_mul_f32 v[160:161], v[118:119], v[126:127] op_sel:[1,1] op_sel_hi:[1,0]
	v_mul_f32_e32 v130, v121, v129
	v_mul_f32_e32 v162, v121, v128
	s_waitcnt vmcnt(7)
	v_mov_b32_e32 v136, v220
	v_mov_b32_e32 v137, v221
	v_mov_b32_e32 v138, v222
	v_mov_b32_e32 v139, v223
	v_pk_mul_f32 v[170:171], v[114:115], v[136:137] op_sel:[1,1] op_sel_hi:[1,0]
	v_mul_f32_e32 v172, v117, v139
	v_mul_f32_e32 v174, v117, v138
	v_pk_mul_f32 v[158:159], v[118:119], v[126:127]
	v_pk_mul_f32 v[168:169], v[114:115], v[136:137]
	v_pk_fma_f32 v[118:119], v[118:119], v[126:127], v[160:161] op_sel_hi:[0,1,1]
	v_pk_fma_f32 v[126:127], v[120:121], v[128:129], v[130:131] op_sel_hi:[1,1,0] neg_lo:[0,0,1] neg_hi:[0,0,1]
	v_pk_fma_f32 v[128:129], v[120:121], v[128:129], v[162:163] op_sel:[0,1,0] op_sel_hi:[1,0,0]
	v_pk_fma_f32 v[114:115], v[114:115], v[136:137], v[170:171] op_sel_hi:[0,1,1]
	v_pk_fma_f32 v[136:137], v[116:117], v[138:139], v[172:173] op_sel_hi:[1,1,0] neg_lo:[0,0,1] neg_hi:[0,0,1]
	v_pk_fma_f32 v[138:139], v[116:117], v[138:139], v[174:175] op_sel:[0,1,0] op_sel_hi:[1,0,0]
	v_sub_f32_e32 v118, v158, v160
	v_sub_f32_e32 v114, v168, v170
	v_mov_b32_e32 v120, v126
	v_mov_b32_e32 v121, v128
	v_mov_b32_e32 v116, v136
	v_mov_b32_e32 v117, v138
.LBB0_1269:
	s_or_b64 exec, exec, s[8:9]
	v_cvt_pk_bf16_f32 v118, v118, v119
	v_cvt_pk_bf16_f32 v119, v120, v121
	v_cvt_pk_bf16_f32 v120, v114, v115
	v_add_u32_e32 v114, 16, v134
	v_ashrrev_i32_e32 v115, 31, v114
	v_cvt_pk_bf16_f32 v121, v116, v117
	v_lshlrev_b64 v[116:117], 6, v[114:115]
	global_store_dwordx4 v[122:123], v[118:121], off offset:256
	s_nop 1
	v_add_u32_e32 v250, 128, v134
	v_lshlrev_b32_e32 v250, 6, v250
	global_load_dwordx4 v[182:185], v250, s[10:11]
	global_load_dwordx4 v[186:189], v250, s[10:11] offset:16
	v_add_u32_e32 v251, 128, v134
	v_lshlrev_b32_e32 v251, 4, v251
	v_and_b32_e32 v251, 0xfff0, v251
	v_add_lshl_u32 v251, v251, v255, 4
	global_load_dwordx4 v[216:219], v251, s[38:39]
	global_load_dwordx4 v[220:223], v251, s[38:39] offset:16
	s_nop 1
	v_lshl_add_u64 v[120:121], s[10:11], 0, v[116:117]
	s_nop 0
	s_waitcnt vmcnt(18)
	v_mov_b32_e32 v116, v190
	v_mov_b32_e32 v117, v191
	v_mov_b32_e32 v118, v192
	v_mov_b32_e32 v119, v193
	v_mov_b32_e32 v126, v116
	v_mov_b32_e32 v120, v194
	v_mov_b32_e32 v121, v195
	v_mov_b32_e32 v122, v196
	v_mov_b32_e32 v123, v197
	v_mov_b32_e32 v127, v120
	v_mov_b32_e32 v120, v117
	v_mov_b32_e32 v116, v118
	v_mov_b32_e32 v117, v122
	v_mov_b32_e32 v122, v119
	v_pk_add_f32 v[118:119], v[126:127], v[120:121]
	v_pk_add_f32 v[116:117], v[116:117], v[122:123]
	s_nop 0
	v_pk_add_f32 v[116:117], v[118:119], v[116:117]
	s_nop 0
	v_add_f32_e32 v115, v116, v117
	v_fmamk_f32 v115, v115, 0x3b000000, v155
	v_mul_f32_e32 v116, 0x4f800000, v115
	v_cmp_gt_f32_e32 vcc, s89, v115
	v_lshlrev_b32_e32 v117, 4, v114
	s_nop 0
	v_cndmask_b32_e32 v115, v115, v116, vcc
	v_sqrt_f32_e32 v116, v115
	s_nop 0
	v_add_u32_e32 v118, -1, v116
	v_add_u32_e32 v119, 1, v116
	v_fma_f32 v120, -v118, v116, v115
	v_fma_f32 v121, -v119, v116, v115
	v_cmp_ge_f32_e64 s[8:9], 0, v120
	s_nop 1
	v_cndmask_b32_e64 v116, v116, v118, s[8:9]
	v_cmp_lt_f32_e64 s[8:9], 0, v121
	s_nop 1
	v_cndmask_b32_e64 v116, v116, v119, s[8:9]
	v_mul_f32_e32 v118, 0x37800000, v116
	v_cndmask_b32_e32 v116, v116, v118, vcc
	v_cmp_class_f32_e32 vcc, v115, v156
	s_nop 1
	v_cndmask_b32_e32 v116, v116, v115, vcc
	v_div_scale_f32 v118, s[8:9], v116, v116, 1.0
	v_rcp_f32_e32 v119, v118
	v_and_b32_e32 v115, 0xfff0, v117
	v_div_scale_f32 v117, vcc, 1.0, v116, 1.0
	v_fma_f32 v120, -v118, v119, 1.0
	v_fmac_f32_e32 v119, v120, v119
	v_mul_f32_e32 v120, v117, v119
	v_fma_f32 v121, -v118, v120, v117
	v_fmac_f32_e32 v120, v121, v119
	v_fma_f32 v117, -v118, v120, v117
	v_div_fmas_f32 v117, v117, v119, v120
	v_div_fixup_f32 v116, v117, v116, 1.0
	v_pk_mul_f32 v[112:113], v[112:113], v[116:117] op_sel_hi:[1,0]
	v_pk_mul_f32 v[110:111], v[110:111], v[116:117] op_sel_hi:[1,0]
	v_pk_mul_f32 v[118:119], v[108:109], v[116:117] op_sel_hi:[1,0]
	v_pk_mul_f32 v[108:109], v[106:107], v[116:117] op_sel_hi:[1,0]
	s_and_saveexec_b64 s[8:9], s[4:5]
	s_cbranch_execz .LBB0_1271
	v_add_u32_e32 v130, v135, v115
	v_lshl_add_u64 v[106:107], v[130:131], 4, s[38:39]
	s_waitcnt vmcnt(11)
	v_mov_b32_e32 v120, v224
	v_mov_b32_e32 v121, v225
	v_mov_b32_e32 v122, v226
	v_mov_b32_e32 v123, v227
	v_pk_mul_f32 v[136:137], v[110:111], v[120:121] op_sel:[1,1] op_sel_hi:[1,0]
	v_mul_f32_e32 v130, v113, v123
	v_mul_f32_e32 v138, v113, v122
	s_waitcnt vmcnt(10)
	v_mov_b32_e32 v126, v228
	v_mov_b32_e32 v127, v229
	v_mov_b32_e32 v128, v230
	v_mov_b32_e32 v129, v231
	v_pk_mul_f32 v[160:161], v[108:109], v[126:127] op_sel:[1,1] op_sel_hi:[1,0]
	v_mul_f32_e32 v162, v119, v129
	v_mul_f32_e32 v168, v119, v128
	v_pk_mul_f32 v[106:107], v[110:111], v[120:121]
	v_pk_mul_f32 v[158:159], v[108:109], v[126:127]
	v_pk_fma_f32 v[110:111], v[110:111], v[120:121], v[136:137] op_sel_hi:[0,1,1]
	v_pk_fma_f32 v[120:121], v[112:113], v[122:123], v[130:131] op_sel_hi:[1,1,0] neg_lo:[0,0,1] neg_hi:[0,0,1]
	v_pk_fma_f32 v[122:123], v[112:113], v[122:123], v[138:139] op_sel:[0,1,0] op_sel_hi:[1,0,0]
	v_pk_fma_f32 v[108:109], v[108:109], v[126:127], v[160:161] op_sel_hi:[0,1,1]
	v_pk_fma_f32 v[126:127], v[118:119], v[128:129], v[162:163] op_sel_hi:[1,1,0] neg_lo:[0,0,1] neg_hi:[0,0,1]
	v_pk_fma_f32 v[128:129], v[118:119], v[128:129], v[168:169] op_sel:[0,1,0] op_sel_hi:[1,0,0]
	v_sub_f32_e32 v110, v106, v136
	v_sub_f32_e32 v108, v158, v160
	v_mov_b32_e32 v112, v120
	v_mov_b32_e32 v113, v122
	v_mov_b32_e32 v118, v126
	v_mov_b32_e32 v119, v128
; __device__ __forceinline__ u32x4 pack8(f32x4 a, f32x4 b) { u32x4 w; w.x = cvtpk(a[0], a[1]); w.y = cvtpk(a[2], a[3]); w.z = cvtpk(b[0], b[1]); w.w = cvtpk(b[2], b[3]); return w; }
;     __device__ __forceinline__ void operator()(const Acc& acc, const Unit& u, int wr, int wc, int fr, int fq) const {
;     ...
;             for (int m = 0; m < 4; ++m) { const int row = row0 + ai * HALF + m * 16, pos = row & (SEQ - 1); const float rs = latent_rstd(ssp, row, 0); bf16_t* rowp = O + (size_t)row * ldc + col0;
; #pragma unroll
;                 for (int bj = 0; bj < 2; ++bj) { f32x4 v0 = acc[ai][bj][m][0] * rs, v1 = acc[ai][bj][m][1] * rs; const int d = (col0 + bj * HALF) % 192;
;                     if (d >= 128) { const int jj = (d - 128) >> 1; const f32x4 c01 = rope[pos * 16 + (jj >> 1)], c23 = rope[pos * 16 + (jj >> 1) + 1];
;                         f32x4 w0, w1;
;                         w0[0] = v0[0] * c01[0] - v0[1] * c01[1]; w0[1] = v0[0] * c01[1] + v0[1] * c01[0];
;                         w0[2] = v0[2] * c01[2] - v0[3] * c01[3]; w0[3] = v0[2] * c01[3] + v0[3] * c01[2];
;                         w1[0] = v1[0] * c23[0] - v1[1] * c23[1]; w1[1] = v1[0] * c23[1] + v1[1] * c23[0];
;                         w1[2] = v1[2] * c23[2] - v1[3] * c23[3]; w1[3] = v1[2] * c23[3] + v1[3] * c23[2];
;                         v0 = w0; v1 = w1; }
;                     *(u32x4*)(rowp + bj * HALF) = pack8(v0, v1); } }
.LBB0_1271:
	s_or_b64 exec, exec, s[8:9]
	v_mov_b64_e32 v[106:107], s[30:31]
	v_mov_b32_e32 v117, v116
	v_mad_i64_i32 v[106:107], s[8:9], v114, s92, v[106:107]
	v_cvt_pk_bf16_f32 v110, v110, v111
	v_cvt_pk_bf16_f32 v111, v112, v113
	v_cvt_pk_bf16_f32 v112, v108, v109
	v_mov_b32_e32 v108, v116
	v_mov_b32_e32 v109, v116
	v_lshl_add_u64 v[106:107], v[132:133], 1, v[106:107]
	v_pk_mul_f32 v[104:105], v[104:105], v[108:109]
	v_pk_mul_f32 v[102:103], v[102:103], v[116:117]
	v_pk_mul_f32 v[100:101], v[100:101], v[108:109]
	v_pk_mul_f32 v[98:99], v[98:99], v[116:117]
	v_cvt_pk_bf16_f32 v113, v118, v119
	global_store_dwordx4 v[106:107], v[110:113], off
	s_and_saveexec_b64 s[8:9], s[6:7]
	s_cbranch_execz .LBB0_1273
	v_add_u32_e32 v130, v124, v115
	v_lshl_add_u64 v[112:113], v[130:131], 4, s[38:39]
	s_waitcnt vmcnt(12)
	v_mov_b32_e32 v108, v224
	v_mov_b32_e32 v109, v225
	v_mov_b32_e32 v110, v226
	v_mov_b32_e32 v111, v227
	v_pk_mul_f32 v[118:119], v[102:103], v[108:109] op_sel:[1,1] op_sel_hi:[1,0]
	v_mul_f32_e32 v120, v105, v111
	v_mul_f32_e32 v122, v105, v110
	s_waitcnt vmcnt(11)
	v_mov_b32_e32 v112, v228
	v_mov_b32_e32 v113, v229
	v_mov_b32_e32 v114, v230
	v_mov_b32_e32 v115, v231
	v_pk_mul_f32 v[128:129], v[98:99], v[112:113] op_sel:[1,1] op_sel_hi:[1,0]
	v_mul_f32_e32 v130, v101, v115
	v_mul_f32_e32 v136, v101, v114
	v_pk_mul_f32 v[116:117], v[102:103], v[108:109]
	v_pk_mul_f32 v[126:127], v[98:99], v[112:113]
	v_pk_fma_f32 v[102:103], v[102:103], v[108:109], v[118:119] op_sel_hi:[0,1,1]
	v_pk_fma_f32 v[108:109], v[104:105], v[110:111], v[120:121] op_sel_hi:[1,1,0] neg_lo:[0,0,1] neg_hi:[0,0,1]
	v_pk_fma_f32 v[110:111], v[104:105], v[110:111], v[122:123] op_sel:[0,1,0] op_sel_hi:[1,0,0]
	v_pk_fma_f32 v[98:99], v[98:99], v[112:113], v[128:129] op_sel_hi:[0,1,1]
	v_pk_fma_f32 v[112:113], v[100:101], v[114:115], v[130:131] op_sel_hi:[1,1,0] neg_lo:[0,0,1] neg_hi:[0,0,1]
	v_pk_fma_f32 v[114:115], v[100:101], v[114:115], v[136:137] op_sel:[0,1,0] op_sel_hi:[1,0,0]
	v_sub_f32_e32 v102, v116, v118
	v_sub_f32_e32 v98, v126, v128
	v_mov_b32_e32 v104, v108
	v_mov_b32_e32 v105, v110
	v_mov_b32_e32 v100, v112
	v_mov_b32_e32 v101, v114
.LBB0_1273:
	s_or_b64 exec, exec, s[8:9]
	v_cvt_pk_bf16_f32 v102, v102, v103
	v_cvt_pk_bf16_f32 v103, v104, v105
	v_cvt_pk_bf16_f32 v104, v98, v99
	v_add_u32_e32 v98, 32, v134
	v_ashrrev_i32_e32 v99, 31, v98
	v_cvt_pk_bf16_f32 v105, v100, v101
	v_lshlrev_b64 v[100:101], 6, v[98:99]
	global_store_dwordx4 v[106:107], v[102:105], off offset:256
	s_nop 1
	v_add_u32_e32 v250, 144, v134
	v_lshlrev_b32_e32 v250, 6, v250
	global_load_dwordx4 v[190:193], v250, s[10:11]
	global_load_dwordx4 v[194:197], v250, s[10:11] offset:16
	v_add_u32_e32 v251, 144, v134
	v_lshlrev_b32_e32 v251, 4, v251
	v_and_b32_e32 v251, 0xfff0, v251
	v_add_lshl_u32 v251, v251, v255, 4
	global_load_dwordx4 v[224:227], v251, s[38:39]
	global_load_dwordx4 v[228:231], v251, s[38:39] offset:16
	s_nop 1
	v_lshl_add_u64 v[104:105], s[10:11], 0, v[100:101]
	s_nop 0
	s_waitcnt vmcnt(22)
	v_mov_b32_e32 v100, v200
	v_mov_b32_e32 v101, v201
	v_mov_b32_e32 v102, v202
	v_mov_b32_e32 v103, v203
	v_mov_b32_e32 v108, v100
	v_mov_b32_e32 v104, v204
	v_mov_b32_e32 v105, v205
	v_mov_b32_e32 v106, v206
	v_mov_b32_e32 v107, v207
	v_mov_b32_e32 v109, v104
	v_mov_b32_e32 v104, v101
	v_mov_b32_e32 v100, v102
	v_mov_b32_e32 v101, v106
	v_mov_b32_e32 v106, v103
	v_pk_add_f32 v[102:103], v[108:109], v[104:105]
	v_pk_add_f32 v[100:101], v[100:101], v[106:107]
	s_nop 0
	v_pk_add_f32 v[100:101], v[102:103], v[100:101]
	s_nop 0
	v_add_f32_e32 v99, v100, v101
	v_fmamk_f32 v99, v99, 0x3b000000, v155
	v_mul_f32_e32 v100, 0x4f800000, v99
	v_cmp_gt_f32_e32 vcc, s89, v99
	v_lshlrev_b32_e32 v101, 4, v98
	s_nop 0
	v_cndmask_b32_e32 v99, v99, v100, vcc
	v_sqrt_f32_e32 v100, v99
	s_nop 0
	v_add_u32_e32 v102, -1, v100
	v_add_u32_e32 v103, 1, v100
	v_fma_f32 v104, -v102, v100, v99
	v_fma_f32 v105, -v103, v100, v99
	v_cmp_ge_f32_e64 s[8:9], 0, v104
	s_nop 1
	v_cndmask_b32_e64 v100, v100, v102, s[8:9]
	v_cmp_lt_f32_e64 s[8:9], 0, v105
	s_nop 1
	v_cndmask_b32_e64 v100, v100, v103, s[8:9]
	v_mul_f32_e32 v102, 0x37800000, v100
	v_cndmask_b32_e32 v100, v100, v102, vcc
	v_cmp_class_f32_e32 vcc, v99, v156
	s_nop 1
	v_cndmask_b32_e32 v100, v100, v99, vcc
	v_div_scale_f32 v102, s[8:9], v100, v100, 1.0
	v_rcp_f32_e32 v103, v102
	v_and_b32_e32 v99, 0xfff0, v101
	v_div_scale_f32 v101, vcc, 1.0, v100, 1.0
	v_fma_f32 v104, -v102, v103, 1.0
	v_fmac_f32_e32 v103, v104, v103
	v_mul_f32_e32 v104, v101, v103
	v_fma_f32 v105, -v102, v104, v101
	v_fmac_f32_e32 v104, v105, v103
	v_fma_f32 v101, -v102, v104, v101
	v_div_fmas_f32 v101, v101, v103, v104
	v_div_fixup_f32 v100, v101, v100, 1.0
	v_pk_mul_f32 v[96:97], v[96:97], v[100:101] op_sel_hi:[1,0]
	v_pk_mul_f32 v[94:95], v[94:95], v[100:101] op_sel_hi:[1,0]
	v_pk_mul_f32 v[102:103], v[92:93], v[100:101] op_sel_hi:[1,0]
	v_pk_mul_f32 v[92:93], v[90:91], v[100:101] op_sel_hi:[1,0]
	s_and_saveexec_b64 s[8:9], s[4:5]
	s_cbranch_execz .LBB0_1275
	v_add_u32_e32 v130, v135, v99
	v_lshl_add_u64 v[90:91], v[130:131], 4, s[38:39]
	s_waitcnt vmcnt(15)
	v_mov_b32_e32 v104, v232
	v_mov_b32_e32 v105, v233
	v_mov_b32_e32 v106, v234
	v_mov_b32_e32 v107, v235
	v_pk_mul_f32 v[112:113], v[94:95], v[104:105] op_sel:[1,1] op_sel_hi:[1,0]
	v_mul_f32_e32 v114, v97, v107
	v_mul_f32_e32 v116, v97, v106
	s_waitcnt vmcnt(14)
	v_mov_b32_e32 v108, v236
	v_mov_b32_e32 v109, v237
	v_mov_b32_e32 v110, v238
	v_mov_b32_e32 v111, v239
	v_pk_mul_f32 v[120:121], v[92:93], v[108:109] op_sel:[1,1] op_sel_hi:[1,0]
	v_mul_f32_e32 v122, v103, v111
	v_mul_f32_e32 v126, v103, v110
	v_pk_mul_f32 v[90:91], v[94:95], v[104:105]
	v_pk_mul_f32 v[118:119], v[92:93], v[108:109]
	v_pk_fma_f32 v[94:95], v[94:95], v[104:105], v[112:113] op_sel_hi:[0,1,1]
	v_pk_fma_f32 v[104:105], v[96:97], v[106:107], v[114:115] op_sel_hi:[1,1,0] neg_lo:[0,0,1] neg_hi:[0,0,1]
	v_pk_fma_f32 v[106:107], v[96:97], v[106:107], v[116:117] op_sel:[0,1,0] op_sel_hi:[1,0,0]
	v_pk_fma_f32 v[92:93], v[92:93], v[108:109], v[120:121] op_sel_hi:[0,1,1]
	v_pk_fma_f32 v[108:109], v[102:103], v[110:111], v[122:123] op_sel_hi:[1,1,0] neg_lo:[0,0,1] neg_hi:[0,0,1]
	v_pk_fma_f32 v[110:111], v[102:103], v[110:111], v[126:127] op_sel:[0,1,0] op_sel_hi:[1,0,0]
	v_sub_f32_e32 v94, v90, v112
	v_sub_f32_e32 v92, v118, v120
	v_mov_b32_e32 v96, v104
	v_mov_b32_e32 v97, v106
	v_mov_b32_e32 v102, v108
	v_mov_b32_e32 v103, v110
; __device__ __forceinline__ u32x4 pack8(f32x4 a, f32x4 b) { u32x4 w; w.x = cvtpk(a[0], a[1]); w.y = cvtpk(a[2], a[3]); w.z = cvtpk(b[0], b[1]); w.w = cvtpk(b[2], b[3]); return w; }
;     __device__ __forceinline__ void operator()(const Acc& acc, const Unit& u, int wr, int wc, int fr, int fq) const {
;     ...
;             for (int m = 0; m < 4; ++m) { const int row = row0 + ai * HALF + m * 16, pos = row & (SEQ - 1); const float rs = latent_rstd(ssp, row, 0); bf16_t* rowp = O + (size_t)row * ldc + col0;
; #pragma unroll
;                 for (int bj = 0; bj < 2; ++bj) { f32x4 v0 = acc[ai][bj][m][0] * rs, v1 = acc[ai][bj][m][1] * rs; const int d = (col0 + bj * HALF) % 192;
;                     if (d >= 128) { const int jj = (d - 128) >> 1; const f32x4 c01 = rope[pos * 16 + (jj >> 1)], c23 = rope[pos * 16 + (jj >> 1) + 1];
;                         f32x4 w0, w1;
;                         w0[0] = v0[0] * c01[0] - v0[1] * c01[1]; w0[1] = v0[0] * c01[1] + v0[1] * c01[0];
;                         w0[2] = v0[2] * c01[2] - v0[3] * c01[3]; w0[3] = v0[2] * c01[3] + v0[3] * c01[2];
;                         w1[0] = v1[0] * c23[0] - v1[1] * c23[1]; w1[1] = v1[0] * c23[1] + v1[1] * c23[0];
;                         w1[2] = v1[2] * c23[2] - v1[3] * c23[3]; w1[3] = v1[2] * c23[3] + v1[3] * c23[2];
;                         v0 = w0; v1 = w1; }
;                     *(u32x4*)(rowp + bj * HALF) = pack8(v0, v1); } }
.LBB0_1275:
	s_or_b64 exec, exec, s[8:9]
	v_mov_b64_e32 v[90:91], s[30:31]
	v_mov_b32_e32 v101, v100
	v_mad_i64_i32 v[90:91], s[8:9], v98, s92, v[90:91]
	v_cvt_pk_bf16_f32 v94, v94, v95
	v_cvt_pk_bf16_f32 v95, v96, v97
	v_cvt_pk_bf16_f32 v96, v92, v93
	v_mov_b32_e32 v92, v100
	v_mov_b32_e32 v93, v100
	v_lshl_add_u64 v[90:91], v[132:133], 1, v[90:91]
	v_pk_mul_f32 v[88:89], v[88:89], v[92:93]
	v_pk_mul_f32 v[86:87], v[86:87], v[100:101]
	v_pk_mul_f32 v[84:85], v[84:85], v[92:93]
	v_pk_mul_f32 v[82:83], v[82:83], v[100:101]
	v_cvt_pk_bf16_f32 v97, v102, v103
	global_store_dwordx4 v[90:91], v[94:97], off
	s_and_saveexec_b64 s[8:9], s[6:7]
	s_cbranch_execz .LBB0_1277
	v_add_u32_e32 v130, v124, v99
	v_lshl_add_u64 v[96:97], v[130:131], 4, s[38:39]
	s_waitcnt vmcnt(16)
	v_mov_b32_e32 v92, v232
	v_mov_b32_e32 v93, v233
	v_mov_b32_e32 v94, v234
	v_mov_b32_e32 v95, v235
	v_pk_mul_f32 v[102:103], v[86:87], v[92:93] op_sel:[1,1] op_sel_hi:[1,0]
	v_mul_f32_e32 v104, v89, v95
	v_mul_f32_e32 v106, v89, v94
	s_waitcnt vmcnt(15)
	v_mov_b32_e32 v96, v236
	v_mov_b32_e32 v97, v237
	v_mov_b32_e32 v98, v238
	v_mov_b32_e32 v99, v239
	v_pk_mul_f32 v[110:111], v[82:83], v[96:97] op_sel:[1,1] op_sel_hi:[1,0]
	v_mul_f32_e32 v112, v85, v99
	v_mul_f32_e32 v114, v85, v98
	v_pk_mul_f32 v[100:101], v[86:87], v[92:93]
	v_pk_mul_f32 v[108:109], v[82:83], v[96:97]
	v_pk_fma_f32 v[86:87], v[86:87], v[92:93], v[102:103] op_sel_hi:[0,1,1]
	v_pk_fma_f32 v[92:93], v[88:89], v[94:95], v[104:105] op_sel_hi:[1,1,0] neg_lo:[0,0,1] neg_hi:[0,0,1]
	v_pk_fma_f32 v[94:95], v[88:89], v[94:95], v[106:107] op_sel:[0,1,0] op_sel_hi:[1,0,0]
	v_pk_fma_f32 v[82:83], v[82:83], v[96:97], v[110:111] op_sel_hi:[0,1,1]
	v_pk_fma_f32 v[96:97], v[84:85], v[98:99], v[112:113] op_sel_hi:[1,1,0] neg_lo:[0,0,1] neg_hi:[0,0,1]
	v_pk_fma_f32 v[98:99], v[84:85], v[98:99], v[114:115] op_sel:[0,1,0] op_sel_hi:[1,0,0]
	v_sub_f32_e32 v86, v100, v102
	v_sub_f32_e32 v82, v108, v110
	v_mov_b32_e32 v88, v92
	v_mov_b32_e32 v89, v94
	v_mov_b32_e32 v84, v96
	v_mov_b32_e32 v85, v98
.LBB0_1277:
	s_or_b64 exec, exec, s[8:9]
	v_cvt_pk_bf16_f32 v86, v86, v87
	v_cvt_pk_bf16_f32 v87, v88, v89
	v_cvt_pk_bf16_f32 v88, v82, v83
	v_add_u32_e32 v82, 48, v134
	v_ashrrev_i32_e32 v83, 31, v82
	v_cvt_pk_bf16_f32 v89, v84, v85
	v_lshlrev_b64 v[84:85], 6, v[82:83]
	global_store_dwordx4 v[90:91], v[86:89], off offset:256
	s_nop 1
	v_add_u32_e32 v250, 160, v134
	v_lshlrev_b32_e32 v250, 6, v250
	global_load_dwordx4 v[200:203], v250, s[10:11]
	global_load_dwordx4 v[204:207], v250, s[10:11] offset:16
	v_add_u32_e32 v251, 160, v134
	v_lshlrev_b32_e32 v251, 4, v251
	v_and_b32_e32 v251, 0xfff0, v251
	v_add_lshl_u32 v251, v251, v255, 4
	global_load_dwordx4 v[232:235], v251, s[38:39]
	global_load_dwordx4 v[236:239], v251, s[38:39] offset:16
	s_nop 1
	v_lshl_add_u64 v[88:89], s[10:11], 0, v[84:85]
	s_nop 0
	s_waitcnt vmcnt(26)
	v_mov_b32_e32 v84, v208
	v_mov_b32_e32 v85, v209
	v_mov_b32_e32 v86, v210
	v_mov_b32_e32 v87, v211
	v_mov_b32_e32 v92, v84
	v_mov_b32_e32 v88, v212
	v_mov_b32_e32 v89, v213
	v_mov_b32_e32 v90, v214
	v_mov_b32_e32 v91, v215
	v_mov_b32_e32 v93, v88
	v_mov_b32_e32 v88, v85
	v_mov_b32_e32 v84, v86
	v_mov_b32_e32 v85, v90
	v_mov_b32_e32 v90, v87
	v_pk_add_f32 v[86:87], v[92:93], v[88:89]
	v_pk_add_f32 v[84:85], v[84:85], v[90:91]
	s_nop 0
	v_pk_add_f32 v[84:85], v[86:87], v[84:85]
	s_nop 0
	v_add_f32_e32 v83, v84, v85
	v_fmamk_f32 v83, v83, 0x3b000000, v155
	v_mul_f32_e32 v84, 0x4f800000, v83
	v_cmp_gt_f32_e32 vcc, s89, v83
	v_lshlrev_b32_e32 v85, 4, v82
	s_nop 0
	v_cndmask_b32_e32 v83, v83, v84, vcc
	v_sqrt_f32_e32 v84, v83
	s_nop 0
	v_add_u32_e32 v86, -1, v84
	v_add_u32_e32 v87, 1, v84
	v_fma_f32 v88, -v86, v84, v83
	v_fma_f32 v89, -v87, v84, v83
	v_cmp_ge_f32_e64 s[8:9], 0, v88
	s_nop 1
	v_cndmask_b32_e64 v84, v84, v86, s[8:9]
	v_cmp_lt_f32_e64 s[8:9], 0, v89
	s_nop 1
	v_cndmask_b32_e64 v84, v84, v87, s[8:9]
	v_mul_f32_e32 v86, 0x37800000, v84
	v_cndmask_b32_e32 v84, v84, v86, vcc
	v_cmp_class_f32_e32 vcc, v83, v156
	s_nop 1
	v_cndmask_b32_e32 v84, v84, v83, vcc
	v_div_scale_f32 v86, s[8:9], v84, v84, 1.0
	v_rcp_f32_e32 v87, v86
	v_and_b32_e32 v83, 0xfff0, v85
	v_div_scale_f32 v85, vcc, 1.0, v84, 1.0
	v_fma_f32 v88, -v86, v87, 1.0
	v_fmac_f32_e32 v87, v88, v87
	v_mul_f32_e32 v88, v85, v87
	v_fma_f32 v89, -v86, v88, v85
	v_fmac_f32_e32 v88, v89, v87
	v_fma_f32 v85, -v86, v88, v85
	v_div_fmas_f32 v85, v85, v87, v88
	v_div_fixup_f32 v84, v85, v84, 1.0
	v_pk_mul_f32 v[80:81], v[80:81], v[84:85] op_sel_hi:[1,0]
	v_pk_mul_f32 v[78:79], v[78:79], v[84:85] op_sel_hi:[1,0]
	v_pk_mul_f32 v[86:87], v[76:77], v[84:85] op_sel_hi:[1,0]
	v_pk_mul_f32 v[76:77], v[74:75], v[84:85] op_sel_hi:[1,0]
	s_and_saveexec_b64 s[8:9], s[4:5]
	s_cbranch_execz .LBB0_1279
	v_add_u32_e32 v130, v135, v83
	v_lshl_add_u64 v[74:75], v[130:131], 4, s[38:39]
	s_waitcnt vmcnt(19)
	v_mov_b32_e32 v88, v240
	v_mov_b32_e32 v89, v241
	v_mov_b32_e32 v90, v242
	v_mov_b32_e32 v91, v243
	v_pk_mul_f32 v[96:97], v[78:79], v[88:89] op_sel:[1,1] op_sel_hi:[1,0]
	v_mul_f32_e32 v98, v81, v91
	v_mul_f32_e32 v100, v81, v90
	s_waitcnt vmcnt(18)
	v_mov_b32_e32 v92, v244
	v_mov_b32_e32 v93, v245
	v_mov_b32_e32 v94, v246
	v_mov_b32_e32 v95, v247
	v_pk_mul_f32 v[104:105], v[76:77], v[92:93] op_sel:[1,1] op_sel_hi:[1,0]
	v_mul_f32_e32 v106, v87, v95
	v_mul_f32_e32 v108, v87, v94
	v_pk_mul_f32 v[74:75], v[78:79], v[88:89]
	v_pk_mul_f32 v[102:103], v[76:77], v[92:93]
	v_pk_fma_f32 v[78:79], v[78:79], v[88:89], v[96:97] op_sel_hi:[0,1,1]
	v_pk_fma_f32 v[88:89], v[80:81], v[90:91], v[98:99] op_sel_hi:[1,1,0] neg_lo:[0,0,1] neg_hi:[0,0,1]
	v_pk_fma_f32 v[90:91], v[80:81], v[90:91], v[100:101] op_sel:[0,1,0] op_sel_hi:[1,0,0]
	v_pk_fma_f32 v[76:77], v[76:77], v[92:93], v[104:105] op_sel_hi:[0,1,1]
	v_pk_fma_f32 v[92:93], v[86:87], v[94:95], v[106:107] op_sel_hi:[1,1,0] neg_lo:[0,0,1] neg_hi:[0,0,1]
	v_pk_fma_f32 v[94:95], v[86:87], v[94:95], v[108:109] op_sel:[0,1,0] op_sel_hi:[1,0,0]
	v_sub_f32_e32 v78, v74, v96
	v_sub_f32_e32 v76, v102, v104
	v_mov_b32_e32 v80, v88
	v_mov_b32_e32 v81, v90
	v_mov_b32_e32 v86, v92
	v_mov_b32_e32 v87, v94
; __device__ __forceinline__ u32x4 pack8(f32x4 a, f32x4 b) { u32x4 w; w.x = cvtpk(a[0], a[1]); w.y = cvtpk(a[2], a[3]); w.z = cvtpk(b[0], b[1]); w.w = cvtpk(b[2], b[3]); return w; }
; __device__ __forceinline__ float latent_rstd(const float* ssp, int row, int which) {
;     const f32x4 a = *(const f32x4*)(ssp + ((size_t)row * 2 + which) * 8), b = *(const f32x4*)(ssp + ((size_t)row * 2 + which) * 8 + 4);
;     return 1.0f / sqrtf((((a[0] + a[1]) + (a[2] + a[3])) + ((b[0] + b[1]) + (b[2] + b[3]))) * (1.0f / 512.0f) + 1e-6f);
;     __device__ __forceinline__ void operator()(const Acc& acc, const Unit& u, int wr, int wc, int fr, int fq) const {
;     ...
;             for (int m = 0; m < 4; ++m) { const int row = row0 + ai * HALF + m * 16, pos = row & (SEQ - 1); const float rs = latent_rstd(ssp, row, 0); bf16_t* rowp = O + (size_t)row * ldc + col0;
; #pragma unroll
;                 for (int bj = 0; bj < 2; ++bj) { f32x4 v0 = acc[ai][bj][m][0] * rs, v1 = acc[ai][bj][m][1] * rs; const int d = (col0 + bj * HALF) % 192;
;                     if (d >= 128) { const int jj = (d - 128) >> 1; const f32x4 c01 = rope[pos * 16 + (jj >> 1)], c23 = rope[pos * 16 + (jj >> 1) + 1];
;                         f32x4 w0, w1;
;                         w0[0] = v0[0] * c01[0] - v0[1] * c01[1]; w0[1] = v0[0] * c01[1] + v0[1] * c01[0];
;                         w0[2] = v0[2] * c01[2] - v0[3] * c01[3]; w0[3] = v0[2] * c01[3] + v0[3] * c01[2];
;                         w1[0] = v1[0] * c23[0] - v1[1] * c23[1]; w1[1] = v1[0] * c23[1] + v1[1] * c23[0];
;                         w1[2] = v1[2] * c23[2] - v1[3] * c23[3]; w1[3] = v1[2] * c23[3] + v1[3] * c23[2];
;                         v0 = w0; v1 = w1; }
;                     *(u32x4*)(rowp + bj * HALF) = pack8(v0, v1); } }
.LBB0_1279:
	s_or_b64 exec, exec, s[8:9]
	v_mov_b64_e32 v[74:75], s[30:31]
	v_mov_b32_e32 v85, v84
	v_mad_i64_i32 v[74:75], s[8:9], v82, s92, v[74:75]
	v_cvt_pk_bf16_f32 v78, v78, v79
	v_cvt_pk_bf16_f32 v79, v80, v81
	v_cvt_pk_bf16_f32 v80, v76, v77
	v_mov_b32_e32 v76, v84
	v_mov_b32_e32 v77, v84
	v_lshl_add_u64 v[74:75], v[132:133], 1, v[74:75]
	v_pk_mul_f32 v[72:73], v[72:73], v[76:77]
	v_pk_mul_f32 v[70:71], v[70:71], v[84:85]
	v_pk_mul_f32 v[68:69], v[68:69], v[76:77]
	v_pk_mul_f32 v[66:67], v[66:67], v[84:85]
	v_cvt_pk_bf16_f32 v81, v86, v87
	global_store_dwordx4 v[74:75], v[78:81], off
	s_and_saveexec_b64 s[8:9], s[6:7]
	s_cbranch_execz .LBB0_1281
	v_add_u32_e32 v130, v124, v83
	v_lshl_add_u64 v[80:81], v[130:131], 4, s[38:39]
	s_waitcnt vmcnt(20)
	v_mov_b32_e32 v76, v240
	v_mov_b32_e32 v77, v241
	v_mov_b32_e32 v78, v242
	v_mov_b32_e32 v79, v243
	v_pk_mul_f32 v[86:87], v[70:71], v[76:77] op_sel:[1,1] op_sel_hi:[1,0]
	v_mul_f32_e32 v88, v73, v79
	v_mul_f32_e32 v90, v73, v78
	s_waitcnt vmcnt(19)
	v_mov_b32_e32 v80, v244
	v_mov_b32_e32 v81, v245
	v_mov_b32_e32 v82, v246
	v_mov_b32_e32 v83, v247
	v_pk_mul_f32 v[94:95], v[66:67], v[80:81] op_sel:[1,1] op_sel_hi:[1,0]
	v_mul_f32_e32 v96, v69, v83
	v_mul_f32_e32 v98, v69, v82
	v_pk_mul_f32 v[84:85], v[70:71], v[76:77]
	v_pk_mul_f32 v[92:93], v[66:67], v[80:81]
	v_pk_fma_f32 v[70:71], v[70:71], v[76:77], v[86:87] op_sel_hi:[0,1,1]
	v_pk_fma_f32 v[76:77], v[72:73], v[78:79], v[88:89] op_sel_hi:[1,1,0] neg_lo:[0,0,1] neg_hi:[0,0,1]
	v_pk_fma_f32 v[78:79], v[72:73], v[78:79], v[90:91] op_sel:[0,1,0] op_sel_hi:[1,0,0]
	v_pk_fma_f32 v[66:67], v[66:67], v[80:81], v[94:95] op_sel_hi:[0,1,1]
	v_pk_fma_f32 v[80:81], v[68:69], v[82:83], v[96:97] op_sel_hi:[1,1,0] neg_lo:[0,0,1] neg_hi:[0,0,1]
	v_pk_fma_f32 v[82:83], v[68:69], v[82:83], v[98:99] op_sel:[0,1,0] op_sel_hi:[1,0,0]
	v_sub_f32_e32 v70, v84, v86
	v_sub_f32_e32 v66, v92, v94
	v_mov_b32_e32 v72, v76
	v_mov_b32_e32 v73, v78
	v_mov_b32_e32 v68, v80
	v_mov_b32_e32 v69, v82
.LBB0_1281:
	s_or_b64 exec, exec, s[8:9]
	v_cvt_pk_bf16_f32 v70, v70, v71
	v_cvt_pk_bf16_f32 v71, v72, v73
	v_cvt_pk_bf16_f32 v72, v66, v67
	v_add_u32_e32 v66, 0x80, v134
	v_ashrrev_i32_e32 v67, 31, v66
	v_cvt_pk_bf16_f32 v73, v68, v69
	v_lshlrev_b64 v[68:69], 6, v[66:67]
	global_store_dwordx4 v[74:75], v[70:73], off offset:256
	s_nop 1
	v_add_u32_e32 v250, 176, v134
	v_lshlrev_b32_e32 v250, 6, v250
	global_load_dwordx4 v[208:211], v250, s[10:11]
	global_load_dwordx4 v[212:215], v250, s[10:11] offset:16
	v_add_u32_e32 v251, 176, v134
	v_lshlrev_b32_e32 v251, 4, v251
	v_and_b32_e32 v251, 0xfff0, v251
	v_add_lshl_u32 v251, v251, v255, 4
	global_load_dwordx4 v[240:243], v251, s[38:39]
	global_load_dwordx4 v[244:247], v251, s[38:39] offset:16
	s_nop 1
	v_lshl_add_u64 v[72:73], s[10:11], 0, v[68:69]
	s_nop 0
	s_waitcnt vmcnt(20)
	v_mov_b32_e32 v68, v182
	v_mov_b32_e32 v69, v183
	v_mov_b32_e32 v70, v184
	v_mov_b32_e32 v71, v185
	v_mov_b32_e32 v76, v68
	v_mov_b32_e32 v72, v186
	v_mov_b32_e32 v73, v187
	v_mov_b32_e32 v74, v188
	v_mov_b32_e32 v75, v189
	v_mov_b32_e32 v77, v72
	v_mov_b32_e32 v72, v69
	v_mov_b32_e32 v68, v70
	v_mov_b32_e32 v69, v74
	v_mov_b32_e32 v74, v71
	v_pk_add_f32 v[70:71], v[76:77], v[72:73]
	v_pk_add_f32 v[68:69], v[68:69], v[74:75]
	s_nop 0
	v_pk_add_f32 v[68:69], v[70:71], v[68:69]
	s_nop 0
	v_add_f32_e32 v67, v68, v69
	v_fmamk_f32 v67, v67, 0x3b000000, v155
	v_mul_f32_e32 v68, 0x4f800000, v67
	v_cmp_gt_f32_e32 vcc, s89, v67
	v_lshlrev_b32_e32 v69, 4, v66
	s_nop 0
	v_cndmask_b32_e32 v67, v67, v68, vcc
	v_sqrt_f32_e32 v68, v67
	s_nop 0
	v_add_u32_e32 v70, -1, v68
	v_add_u32_e32 v71, 1, v68
	v_fma_f32 v72, -v70, v68, v67
	v_fma_f32 v73, -v71, v68, v67
	v_cmp_ge_f32_e64 s[8:9], 0, v72
	s_nop 1
	v_cndmask_b32_e64 v68, v68, v70, s[8:9]
	v_cmp_lt_f32_e64 s[8:9], 0, v73
	s_nop 1
	v_cndmask_b32_e64 v68, v68, v71, s[8:9]
	v_mul_f32_e32 v70, 0x37800000, v68
	v_cndmask_b32_e32 v68, v68, v70, vcc
	v_cmp_class_f32_e32 vcc, v67, v156
	s_nop 1
	v_cndmask_b32_e32 v68, v68, v67, vcc
	v_div_scale_f32 v70, s[8:9], v68, v68, 1.0
	v_rcp_f32_e32 v71, v70
	v_and_b32_e32 v67, 0xfff0, v69
	v_div_scale_f32 v69, vcc, 1.0, v68, 1.0
	v_fma_f32 v72, -v70, v71, 1.0
	v_fmac_f32_e32 v71, v72, v71
	v_mul_f32_e32 v72, v69, v71
	v_fma_f32 v73, -v70, v72, v69
	v_fmac_f32_e32 v72, v73, v71
	v_fma_f32 v69, -v70, v72, v69
	v_div_fmas_f32 v69, v69, v71, v72
	v_div_fixup_f32 v68, v69, v68, 1.0
	v_pk_mul_f32 v[64:65], v[64:65], v[68:69] op_sel_hi:[1,0]
	v_pk_mul_f32 v[62:63], v[62:63], v[68:69] op_sel_hi:[1,0]
	v_pk_mul_f32 v[70:71], v[60:61], v[68:69] op_sel_hi:[1,0]
	v_pk_mul_f32 v[60:61], v[58:59], v[68:69] op_sel_hi:[1,0]
	s_and_saveexec_b64 s[8:9], s[4:5]
	s_cbranch_execz .LBB0_1283
	v_add_u32_e32 v130, v135, v67
	v_lshl_add_u64 v[58:59], v[130:131], 4, s[38:39]
	s_waitcnt vmcnt(19)
	v_mov_b32_e32 v72, v216
	v_mov_b32_e32 v73, v217
	v_mov_b32_e32 v74, v218
	v_mov_b32_e32 v75, v219
	v_pk_mul_f32 v[80:81], v[62:63], v[72:73] op_sel:[1,1] op_sel_hi:[1,0]
	v_mul_f32_e32 v82, v65, v75
	v_mul_f32_e32 v84, v65, v74
	s_waitcnt vmcnt(18)
	v_mov_b32_e32 v76, v220
	v_mov_b32_e32 v77, v221
	v_mov_b32_e32 v78, v222
	v_mov_b32_e32 v79, v223
	v_pk_mul_f32 v[88:89], v[60:61], v[76:77] op_sel:[1,1] op_sel_hi:[1,0]
	v_mul_f32_e32 v90, v71, v79
	v_mul_f32_e32 v92, v71, v78
	v_pk_mul_f32 v[58:59], v[62:63], v[72:73]
	v_pk_mul_f32 v[86:87], v[60:61], v[76:77]
	v_pk_fma_f32 v[62:63], v[62:63], v[72:73], v[80:81] op_sel_hi:[0,1,1]
	v_pk_fma_f32 v[72:73], v[64:65], v[74:75], v[82:83] op_sel_hi:[1,1,0] neg_lo:[0,0,1] neg_hi:[0,0,1]
	v_pk_fma_f32 v[74:75], v[64:65], v[74:75], v[84:85] op_sel:[0,1,0] op_sel_hi:[1,0,0]
	v_pk_fma_f32 v[60:61], v[60:61], v[76:77], v[88:89] op_sel_hi:[0,1,1]
	v_pk_fma_f32 v[76:77], v[70:71], v[78:79], v[90:91] op_sel_hi:[1,1,0] neg_lo:[0,0,1] neg_hi:[0,0,1]
	v_pk_fma_f32 v[78:79], v[70:71], v[78:79], v[92:93] op_sel:[0,1,0] op_sel_hi:[1,0,0]
	v_sub_f32_e32 v62, v58, v80
	v_sub_f32_e32 v60, v86, v88
	v_mov_b32_e32 v64, v72
	v_mov_b32_e32 v65, v74
	v_mov_b32_e32 v70, v76
	v_mov_b32_e32 v71, v78
; __device__ __forceinline__ u32x4 pack8(f32x4 a, f32x4 b) { u32x4 w; w.x = cvtpk(a[0], a[1]); w.y = cvtpk(a[2], a[3]); w.z = cvtpk(b[0], b[1]); w.w = cvtpk(b[2], b[3]); return w; }
; __device__ __forceinline__ float latent_rstd(const float* ssp, int row, int which) {
;     const f32x4 a = *(const f32x4*)(ssp + ((size_t)row * 2 + which) * 8), b = *(const f32x4*)(ssp + ((size_t)row * 2 + which) * 8 + 4);
;     return 1.0f / sqrtf((((a[0] + a[1]) + (a[2] + a[3])) + ((b[0] + b[1]) + (b[2] + b[3]))) * (1.0f / 512.0f) + 1e-6f);
;     __device__ __forceinline__ void operator()(const Acc& acc, const Unit& u, int wr, int wc, int fr, int fq) const {
;     ...
;             for (int m = 0; m < 4; ++m) { const int row = row0 + ai * HALF + m * 16, pos = row & (SEQ - 1); const float rs = latent_rstd(ssp, row, 0); bf16_t* rowp = O + (size_t)row * ldc + col0;
; #pragma unroll
;                 for (int bj = 0; bj < 2; ++bj) { f32x4 v0 = acc[ai][bj][m][0] * rs, v1 = acc[ai][bj][m][1] * rs; const int d = (col0 + bj * HALF) % 192;
;                     if (d >= 128) { const int jj = (d - 128) >> 1; const f32x4 c01 = rope[pos * 16 + (jj >> 1)], c23 = rope[pos * 16 + (jj >> 1) + 1];
;                         f32x4 w0, w1;
;                         w0[0] = v0[0] * c01[0] - v0[1] * c01[1]; w0[1] = v0[0] * c01[1] + v0[1] * c01[0];
;                         w0[2] = v0[2] * c01[2] - v0[3] * c01[3]; w0[3] = v0[2] * c01[3] + v0[3] * c01[2];
;                         w1[0] = v1[0] * c23[0] - v1[1] * c23[1]; w1[1] = v1[0] * c23[1] + v1[1] * c23[0];
;                         w1[2] = v1[2] * c23[2] - v1[3] * c23[3]; w1[3] = v1[2] * c23[3] + v1[3] * c23[2];
;                         v0 = w0; v1 = w1; }
;                     *(u32x4*)(rowp + bj * HALF) = pack8(v0, v1); } }
.LBB0_1283:
	s_or_b64 exec, exec, s[8:9]
	v_mov_b64_e32 v[58:59], s[30:31]
	v_mov_b32_e32 v69, v68
	v_mad_i64_i32 v[58:59], s[8:9], v66, s92, v[58:59]
	v_cvt_pk_bf16_f32 v62, v62, v63
	v_cvt_pk_bf16_f32 v63, v64, v65
	v_cvt_pk_bf16_f32 v64, v60, v61
	v_mov_b32_e32 v60, v68
	v_mov_b32_e32 v61, v68
	v_lshl_add_u64 v[58:59], v[132:133], 1, v[58:59]
	v_pk_mul_f32 v[56:57], v[56:57], v[60:61]
	v_pk_mul_f32 v[54:55], v[54:55], v[68:69]
	v_pk_mul_f32 v[52:53], v[52:53], v[60:61]
	v_pk_mul_f32 v[50:51], v[50:51], v[68:69]
	v_cvt_pk_bf16_f32 v65, v70, v71
	global_store_dwordx4 v[58:59], v[62:65], off
	s_and_saveexec_b64 s[8:9], s[6:7]
	s_cbranch_execz .LBB0_1285
	v_add_u32_e32 v130, v124, v67
	v_lshl_add_u64 v[64:65], v[130:131], 4, s[38:39]
	s_waitcnt vmcnt(20)
	v_mov_b32_e32 v60, v216
	v_mov_b32_e32 v61, v217
	v_mov_b32_e32 v62, v218
	v_mov_b32_e32 v63, v219
	v_pk_mul_f32 v[70:71], v[54:55], v[60:61] op_sel:[1,1] op_sel_hi:[1,0]
	v_mul_f32_e32 v72, v57, v63
	v_mul_f32_e32 v74, v57, v62
	s_waitcnt vmcnt(19)
	v_mov_b32_e32 v64, v220
	v_mov_b32_e32 v65, v221
	v_mov_b32_e32 v66, v222
	v_mov_b32_e32 v67, v223
	v_pk_mul_f32 v[78:79], v[50:51], v[64:65] op_sel:[1,1] op_sel_hi:[1,0]
	v_mul_f32_e32 v80, v53, v67
	v_mul_f32_e32 v82, v53, v66
	v_pk_mul_f32 v[68:69], v[54:55], v[60:61]
	v_pk_mul_f32 v[76:77], v[50:51], v[64:65]
	v_pk_fma_f32 v[54:55], v[54:55], v[60:61], v[70:71] op_sel_hi:[0,1,1]
	v_pk_fma_f32 v[60:61], v[56:57], v[62:63], v[72:73] op_sel_hi:[1,1,0] neg_lo:[0,0,1] neg_hi:[0,0,1]
	v_pk_fma_f32 v[62:63], v[56:57], v[62:63], v[74:75] op_sel:[0,1,0] op_sel_hi:[1,0,0]
	v_pk_fma_f32 v[50:51], v[50:51], v[64:65], v[78:79] op_sel_hi:[0,1,1]
	v_pk_fma_f32 v[64:65], v[52:53], v[66:67], v[80:81] op_sel_hi:[1,1,0] neg_lo:[0,0,1] neg_hi:[0,0,1]
	v_pk_fma_f32 v[66:67], v[52:53], v[66:67], v[82:83] op_sel:[0,1,0] op_sel_hi:[1,0,0]
	v_sub_f32_e32 v54, v68, v70
	v_sub_f32_e32 v50, v76, v78
	v_mov_b32_e32 v56, v60
	v_mov_b32_e32 v57, v62
	v_mov_b32_e32 v52, v64
	v_mov_b32_e32 v53, v66
.LBB0_1285:
	s_or_b64 exec, exec, s[8:9]
	v_cvt_pk_bf16_f32 v54, v54, v55
	v_cvt_pk_bf16_f32 v55, v56, v57
	v_cvt_pk_bf16_f32 v56, v50, v51
	v_add_u32_e32 v50, 0x90, v134
	v_ashrrev_i32_e32 v51, 31, v50
	v_cvt_pk_bf16_f32 v57, v52, v53
	v_lshlrev_b64 v[52:53], 6, v[50:51]
	global_store_dwordx4 v[58:59], v[54:57], off offset:256
	s_nop 1
	v_lshl_add_u64 v[56:57], s[10:11], 0, v[52:53]
	s_nop 0
	s_waitcnt vmcnt(16)
	v_mov_b32_e32 v52, v190
	v_mov_b32_e32 v53, v191
	v_mov_b32_e32 v54, v192
	v_mov_b32_e32 v55, v193
	v_mov_b32_e32 v60, v52
	v_mov_b32_e32 v56, v194
	v_mov_b32_e32 v57, v195
	v_mov_b32_e32 v58, v196
	v_mov_b32_e32 v59, v197
	v_mov_b32_e32 v61, v56
	v_mov_b32_e32 v56, v53
	v_mov_b32_e32 v52, v54
	v_mov_b32_e32 v53, v58
	v_mov_b32_e32 v58, v55
	v_pk_add_f32 v[54:55], v[60:61], v[56:57]
	v_pk_add_f32 v[52:53], v[52:53], v[58:59]
	s_nop 0
	v_pk_add_f32 v[52:53], v[54:55], v[52:53]
	s_nop 0
	v_add_f32_e32 v51, v52, v53
	v_fmamk_f32 v51, v51, 0x3b000000, v155
	v_mul_f32_e32 v52, 0x4f800000, v51
	v_cmp_gt_f32_e32 vcc, s89, v51
	v_lshlrev_b32_e32 v53, 4, v50
	s_nop 0
	v_cndmask_b32_e32 v51, v51, v52, vcc
	v_sqrt_f32_e32 v52, v51
	s_nop 0
	v_add_u32_e32 v54, -1, v52
	v_add_u32_e32 v55, 1, v52
	v_fma_f32 v56, -v54, v52, v51
	v_fma_f32 v57, -v55, v52, v51
	v_cmp_ge_f32_e64 s[8:9], 0, v56
	s_nop 1
	v_cndmask_b32_e64 v52, v52, v54, s[8:9]
	v_cmp_lt_f32_e64 s[8:9], 0, v57
	s_nop 1
	v_cndmask_b32_e64 v52, v52, v55, s[8:9]
	v_mul_f32_e32 v54, 0x37800000, v52
	v_cndmask_b32_e32 v52, v52, v54, vcc
	v_cmp_class_f32_e32 vcc, v51, v156
	s_nop 1
	v_cndmask_b32_e32 v52, v52, v51, vcc
	v_div_scale_f32 v54, s[8:9], v52, v52, 1.0
	v_rcp_f32_e32 v55, v54
	v_and_b32_e32 v51, 0xfff0, v53
	v_div_scale_f32 v53, vcc, 1.0, v52, 1.0
	v_fma_f32 v56, -v54, v55, 1.0
	v_fmac_f32_e32 v55, v56, v55
	v_mul_f32_e32 v56, v53, v55
	v_fma_f32 v57, -v54, v56, v53
	v_fmac_f32_e32 v56, v57, v55
	v_fma_f32 v53, -v54, v56, v53
	v_div_fmas_f32 v53, v53, v55, v56
	v_div_fixup_f32 v52, v53, v52, 1.0
	v_pk_mul_f32 v[48:49], v[48:49], v[52:53] op_sel_hi:[1,0]
	v_pk_mul_f32 v[46:47], v[46:47], v[52:53] op_sel_hi:[1,0]
	v_pk_mul_f32 v[54:55], v[44:45], v[52:53] op_sel_hi:[1,0]
	v_pk_mul_f32 v[44:45], v[42:43], v[52:53] op_sel_hi:[1,0]
	s_and_saveexec_b64 s[8:9], s[4:5]
	s_cbranch_execz .LBB0_1287
	v_add_u32_e32 v130, v135, v51
	v_lshl_add_u64 v[42:43], v[130:131], 4, s[38:39]
	s_waitcnt vmcnt(15)
	v_mov_b32_e32 v56, v224
	v_mov_b32_e32 v57, v225
	v_mov_b32_e32 v58, v226
	v_mov_b32_e32 v59, v227
	v_pk_mul_f32 v[64:65], v[46:47], v[56:57] op_sel:[1,1] op_sel_hi:[1,0]
	v_mul_f32_e32 v66, v49, v59
	v_mul_f32_e32 v68, v49, v58
	s_waitcnt vmcnt(14)
	v_mov_b32_e32 v60, v228
	v_mov_b32_e32 v61, v229
	v_mov_b32_e32 v62, v230
	v_mov_b32_e32 v63, v231
	v_pk_mul_f32 v[72:73], v[44:45], v[60:61] op_sel:[1,1] op_sel_hi:[1,0]
	v_mul_f32_e32 v74, v55, v63
	v_mul_f32_e32 v76, v55, v62
	v_pk_mul_f32 v[42:43], v[46:47], v[56:57]
	v_pk_mul_f32 v[70:71], v[44:45], v[60:61]
	v_pk_fma_f32 v[46:47], v[46:47], v[56:57], v[64:65] op_sel_hi:[0,1,1]
	v_pk_fma_f32 v[56:57], v[48:49], v[58:59], v[66:67] op_sel_hi:[1,1,0] neg_lo:[0,0,1] neg_hi:[0,0,1]
	v_pk_fma_f32 v[58:59], v[48:49], v[58:59], v[68:69] op_sel:[0,1,0] op_sel_hi:[1,0,0]
	v_pk_fma_f32 v[44:45], v[44:45], v[60:61], v[72:73] op_sel_hi:[0,1,1]
	v_pk_fma_f32 v[60:61], v[54:55], v[62:63], v[74:75] op_sel_hi:[1,1,0] neg_lo:[0,0,1] neg_hi:[0,0,1]
	v_pk_fma_f32 v[62:63], v[54:55], v[62:63], v[76:77] op_sel:[0,1,0] op_sel_hi:[1,0,0]
	v_sub_f32_e32 v46, v42, v64
	v_sub_f32_e32 v44, v70, v72
	v_mov_b32_e32 v48, v56
	v_mov_b32_e32 v49, v58
	v_mov_b32_e32 v54, v60
	v_mov_b32_e32 v55, v62
; __device__ __forceinline__ u32x4 pack8(f32x4 a, f32x4 b) { u32x4 w; w.x = cvtpk(a[0], a[1]); w.y = cvtpk(a[2], a[3]); w.z = cvtpk(b[0], b[1]); w.w = cvtpk(b[2], b[3]); return w; }
; __device__ __forceinline__ float latent_rstd(const float* ssp, int row, int which) {
;     const f32x4 a = *(const f32x4*)(ssp + ((size_t)row * 2 + which) * 8), b = *(const f32x4*)(ssp + ((size_t)row * 2 + which) * 8 + 4);
;     return 1.0f / sqrtf((((a[0] + a[1]) + (a[2] + a[3])) + ((b[0] + b[1]) + (b[2] + b[3]))) * (1.0f / 512.0f) + 1e-6f);
;     __device__ __forceinline__ void operator()(const Acc& acc, const Unit& u, int wr, int wc, int fr, int fq) const {
;     ...
;             for (int m = 0; m < 4; ++m) { const int row = row0 + ai * HALF + m * 16, pos = row & (SEQ - 1); const float rs = latent_rstd(ssp, row, 0); bf16_t* rowp = O + (size_t)row * ldc + col0;
; #pragma unroll
;                 for (int bj = 0; bj < 2; ++bj) { f32x4 v0 = acc[ai][bj][m][0] * rs, v1 = acc[ai][bj][m][1] * rs; const int d = (col0 + bj * HALF) % 192;
;                     if (d >= 128) { const int jj = (d - 128) >> 1; const f32x4 c01 = rope[pos * 16 + (jj >> 1)], c23 = rope[pos * 16 + (jj >> 1) + 1];
;                         f32x4 w0, w1;
;                         w0[0] = v0[0] * c01[0] - v0[1] * c01[1]; w0[1] = v0[0] * c01[1] + v0[1] * c01[0];
;                         w0[2] = v0[2] * c01[2] - v0[3] * c01[3]; w0[3] = v0[2] * c01[3] + v0[3] * c01[2];
;                         w1[0] = v1[0] * c23[0] - v1[1] * c23[1]; w1[1] = v1[0] * c23[1] + v1[1] * c23[0];
;                         w1[2] = v1[2] * c23[2] - v1[3] * c23[3]; w1[3] = v1[2] * c23[3] + v1[3] * c23[2];
;                         v0 = w0; v1 = w1; }
;                     *(u32x4*)(rowp + bj * HALF) = pack8(v0, v1); } }
.LBB0_1287:
	s_or_b64 exec, exec, s[8:9]
	v_mov_b64_e32 v[42:43], s[30:31]
	v_mov_b32_e32 v53, v52
	v_mad_i64_i32 v[42:43], s[8:9], v50, s92, v[42:43]
	v_cvt_pk_bf16_f32 v46, v46, v47
	v_cvt_pk_bf16_f32 v47, v48, v49
	v_cvt_pk_bf16_f32 v48, v44, v45
	v_mov_b32_e32 v44, v52
	v_mov_b32_e32 v45, v52
	v_lshl_add_u64 v[42:43], v[132:133], 1, v[42:43]
	v_pk_mul_f32 v[40:41], v[40:41], v[44:45]
	v_pk_mul_f32 v[38:39], v[38:39], v[52:53]
	v_pk_mul_f32 v[36:37], v[36:37], v[44:45]
	v_pk_mul_f32 v[34:35], v[34:35], v[52:53]
	v_cvt_pk_bf16_f32 v49, v54, v55
	global_store_dwordx4 v[42:43], v[46:49], off
	s_and_saveexec_b64 s[8:9], s[6:7]
	s_cbranch_execz .LBB0_1289
	v_add_u32_e32 v130, v124, v51
	v_lshl_add_u64 v[48:49], v[130:131], 4, s[38:39]
	s_waitcnt vmcnt(16)
	v_mov_b32_e32 v44, v224
	v_mov_b32_e32 v45, v225
	v_mov_b32_e32 v46, v226
	v_mov_b32_e32 v47, v227
	v_pk_mul_f32 v[54:55], v[38:39], v[44:45] op_sel:[1,1] op_sel_hi:[1,0]
	v_mul_f32_e32 v56, v41, v47
	v_mul_f32_e32 v58, v41, v46
	s_waitcnt vmcnt(15)
	v_mov_b32_e32 v48, v228
	v_mov_b32_e32 v49, v229
	v_mov_b32_e32 v50, v230
	v_mov_b32_e32 v51, v231
	v_pk_mul_f32 v[62:63], v[34:35], v[48:49] op_sel:[1,1] op_sel_hi:[1,0]
	v_mul_f32_e32 v64, v37, v51
	v_mul_f32_e32 v66, v37, v50
	v_pk_mul_f32 v[52:53], v[38:39], v[44:45]
	v_pk_mul_f32 v[60:61], v[34:35], v[48:49]
	v_pk_fma_f32 v[38:39], v[38:39], v[44:45], v[54:55] op_sel_hi:[0,1,1]
	v_pk_fma_f32 v[44:45], v[40:41], v[46:47], v[56:57] op_sel_hi:[1,1,0] neg_lo:[0,0,1] neg_hi:[0,0,1]
	v_pk_fma_f32 v[46:47], v[40:41], v[46:47], v[58:59] op_sel:[0,1,0] op_sel_hi:[1,0,0]
	v_pk_fma_f32 v[34:35], v[34:35], v[48:49], v[62:63] op_sel_hi:[0,1,1]
	v_pk_fma_f32 v[48:49], v[36:37], v[50:51], v[64:65] op_sel_hi:[1,1,0] neg_lo:[0,0,1] neg_hi:[0,0,1]
	v_pk_fma_f32 v[50:51], v[36:37], v[50:51], v[66:67] op_sel:[0,1,0] op_sel_hi:[1,0,0]
	v_sub_f32_e32 v38, v52, v54
	v_sub_f32_e32 v34, v60, v62
	v_mov_b32_e32 v40, v44
	v_mov_b32_e32 v41, v46
	v_mov_b32_e32 v36, v48
	v_mov_b32_e32 v37, v50
.LBB0_1289:
	s_or_b64 exec, exec, s[8:9]
	v_cvt_pk_bf16_f32 v38, v38, v39
	v_cvt_pk_bf16_f32 v39, v40, v41
	v_cvt_pk_bf16_f32 v40, v34, v35
	v_add_u32_e32 v34, 0xa0, v134
	v_ashrrev_i32_e32 v35, 31, v34
	v_cvt_pk_bf16_f32 v41, v36, v37
	v_lshlrev_b64 v[36:37], 6, v[34:35]
	global_store_dwordx4 v[42:43], v[38:41], off offset:256
	s_nop 1
	v_lshl_add_u64 v[40:41], s[10:11], 0, v[36:37]
	s_nop 0
	s_waitcnt vmcnt(12)
	v_mov_b32_e32 v36, v200
	v_mov_b32_e32 v37, v201
	v_mov_b32_e32 v38, v202
	v_mov_b32_e32 v39, v203
	v_mov_b32_e32 v44, v36
	v_mov_b32_e32 v40, v204
	v_mov_b32_e32 v41, v205
	v_mov_b32_e32 v42, v206
	v_mov_b32_e32 v43, v207
	v_mov_b32_e32 v45, v40
	v_mov_b32_e32 v40, v37
	v_mov_b32_e32 v36, v38
	v_mov_b32_e32 v37, v42
	v_mov_b32_e32 v42, v39
	v_pk_add_f32 v[38:39], v[44:45], v[40:41]
	v_pk_add_f32 v[36:37], v[36:37], v[42:43]
	s_nop 0
	v_pk_add_f32 v[36:37], v[38:39], v[36:37]
	s_nop 0
	v_add_f32_e32 v35, v36, v37
	v_fmamk_f32 v35, v35, 0x3b000000, v155
	v_mul_f32_e32 v36, 0x4f800000, v35
	v_cmp_gt_f32_e32 vcc, s89, v35
	v_lshlrev_b32_e32 v37, 4, v34
	s_nop 0
	v_cndmask_b32_e32 v35, v35, v36, vcc
	v_sqrt_f32_e32 v36, v35
	s_nop 0
	v_add_u32_e32 v38, -1, v36
	v_add_u32_e32 v39, 1, v36
	v_fma_f32 v40, -v38, v36, v35
	v_fma_f32 v41, -v39, v36, v35
	v_cmp_ge_f32_e64 s[8:9], 0, v40
	s_nop 1
	v_cndmask_b32_e64 v36, v36, v38, s[8:9]
	v_cmp_lt_f32_e64 s[8:9], 0, v41
	s_nop 1
	v_cndmask_b32_e64 v36, v36, v39, s[8:9]
	v_mul_f32_e32 v38, 0x37800000, v36
	v_cndmask_b32_e32 v36, v36, v38, vcc
	v_cmp_class_f32_e32 vcc, v35, v156
	s_nop 1
	v_cndmask_b32_e32 v36, v36, v35, vcc
	v_div_scale_f32 v38, s[8:9], v36, v36, 1.0
	v_rcp_f32_e32 v39, v38
	v_and_b32_e32 v35, 0xfff0, v37
	v_div_scale_f32 v37, vcc, 1.0, v36, 1.0
	v_fma_f32 v40, -v38, v39, 1.0
	v_fmac_f32_e32 v39, v40, v39
	v_mul_f32_e32 v40, v37, v39
	v_fma_f32 v41, -v38, v40, v37
	v_fmac_f32_e32 v40, v41, v39
	v_fma_f32 v37, -v38, v40, v37
	v_div_fmas_f32 v37, v37, v39, v40
	v_div_fixup_f32 v36, v37, v36, 1.0
	v_pk_mul_f32 v[32:33], v[32:33], v[36:37] op_sel_hi:[1,0]
	v_pk_mul_f32 v[30:31], v[30:31], v[36:37] op_sel_hi:[1,0]
	v_pk_mul_f32 v[38:39], v[28:29], v[36:37] op_sel_hi:[1,0]
	v_pk_mul_f32 v[28:29], v[26:27], v[36:37] op_sel_hi:[1,0]
	s_and_saveexec_b64 s[8:9], s[4:5]
	s_cbranch_execz .LBB0_1291
	v_add_u32_e32 v130, v135, v35
	v_lshl_add_u64 v[26:27], v[130:131], 4, s[38:39]
	s_waitcnt vmcnt(11)
	v_mov_b32_e32 v40, v232
	v_mov_b32_e32 v41, v233
	v_mov_b32_e32 v42, v234
	v_mov_b32_e32 v43, v235
	v_pk_mul_f32 v[48:49], v[30:31], v[40:41] op_sel:[1,1] op_sel_hi:[1,0]
	v_mul_f32_e32 v50, v33, v43
	v_mul_f32_e32 v52, v33, v42
	s_waitcnt vmcnt(10)
	v_mov_b32_e32 v44, v236
	v_mov_b32_e32 v45, v237
	v_mov_b32_e32 v46, v238
	v_mov_b32_e32 v47, v239
	v_pk_mul_f32 v[56:57], v[28:29], v[44:45] op_sel:[1,1] op_sel_hi:[1,0]
	v_mul_f32_e32 v58, v39, v47
	v_mul_f32_e32 v60, v39, v46
	v_pk_mul_f32 v[26:27], v[30:31], v[40:41]
	v_pk_mul_f32 v[54:55], v[28:29], v[44:45]
	v_pk_fma_f32 v[30:31], v[30:31], v[40:41], v[48:49] op_sel_hi:[0,1,1]
	v_pk_fma_f32 v[40:41], v[32:33], v[42:43], v[50:51] op_sel_hi:[1,1,0] neg_lo:[0,0,1] neg_hi:[0,0,1]
	v_pk_fma_f32 v[42:43], v[32:33], v[42:43], v[52:53] op_sel:[0,1,0] op_sel_hi:[1,0,0]
	v_pk_fma_f32 v[28:29], v[28:29], v[44:45], v[56:57] op_sel_hi:[0,1,1]
	v_pk_fma_f32 v[44:45], v[38:39], v[46:47], v[58:59] op_sel_hi:[1,1,0] neg_lo:[0,0,1] neg_hi:[0,0,1]
	v_pk_fma_f32 v[46:47], v[38:39], v[46:47], v[60:61] op_sel:[0,1,0] op_sel_hi:[1,0,0]
	v_sub_f32_e32 v30, v26, v48
	v_sub_f32_e32 v28, v54, v56
	v_mov_b32_e32 v32, v40
	v_mov_b32_e32 v33, v42
	v_mov_b32_e32 v38, v44
	v_mov_b32_e32 v39, v46
; __device__ __forceinline__ u32x4 pack8(f32x4 a, f32x4 b) { u32x4 w; w.x = cvtpk(a[0], a[1]); w.y = cvtpk(a[2], a[3]); w.z = cvtpk(b[0], b[1]); w.w = cvtpk(b[2], b[3]); return w; }
;     __device__ __forceinline__ void operator()(const Acc& acc, const Unit& u, int wr, int wc, int fr, int fq) const {
;     ...
;                 for (int bj = 0; bj < 2; ++bj) { f32x4 v0 = acc[ai][bj][m][0] * rs, v1 = acc[ai][bj][m][1] * rs; const int d = (col0 + bj * HALF) % 192;
;                     if (d >= 128) { const int jj = (d - 128) >> 1; const f32x4 c01 = rope[pos * 16 + (jj >> 1)], c23 = rope[pos * 16 + (jj >> 1) + 1];
;                         f32x4 w0, w1;
;                         w0[0] = v0[0] * c01[0] - v0[1] * c01[1]; w0[1] = v0[0] * c01[1] + v0[1] * c01[0];
;                         w0[2] = v0[2] * c01[2] - v0[3] * c01[3]; w0[3] = v0[2] * c01[3] + v0[3] * c01[2];
;                         w1[0] = v1[0] * c23[0] - v1[1] * c23[1]; w1[1] = v1[0] * c23[1] + v1[1] * c23[0];
;                         w1[2] = v1[2] * c23[2] - v1[3] * c23[3]; w1[3] = v1[2] * c23[3] + v1[3] * c23[2];
;                         v0 = w0; v1 = w1; }
;                     *(u32x4*)(rowp + bj * HALF) = pack8(v0, v1); } }
.LBB0_1291:
	s_or_b64 exec, exec, s[8:9]
	v_mov_b64_e32 v[26:27], s[30:31]
	v_mov_b32_e32 v37, v36
	v_mad_i64_i32 v[26:27], s[8:9], v34, s92, v[26:27]
	v_cvt_pk_bf16_f32 v30, v30, v31
	v_cvt_pk_bf16_f32 v31, v32, v33
	v_cvt_pk_bf16_f32 v32, v28, v29
	v_mov_b32_e32 v28, v36
	v_mov_b32_e32 v29, v36
	v_lshl_add_u64 v[26:27], v[132:133], 1, v[26:27]
	v_pk_mul_f32 v[24:25], v[24:25], v[28:29]
	v_pk_mul_f32 v[22:23], v[22:23], v[36:37]
	v_pk_mul_f32 v[20:21], v[20:21], v[28:29]
	v_pk_mul_f32 v[18:19], v[18:19], v[36:37]
	v_cvt_pk_bf16_f32 v33, v38, v39
	global_store_dwordx4 v[26:27], v[30:33], off
	s_and_saveexec_b64 s[8:9], s[6:7]
	s_cbranch_execz .LBB0_1293
	v_add_u32_e32 v130, v124, v35
	v_lshl_add_u64 v[32:33], v[130:131], 4, s[38:39]
	s_waitcnt vmcnt(12)
	v_mov_b32_e32 v28, v232
	v_mov_b32_e32 v29, v233
	v_mov_b32_e32 v30, v234
	v_mov_b32_e32 v31, v235
	v_pk_mul_f32 v[38:39], v[22:23], v[28:29] op_sel:[1,1] op_sel_hi:[1,0]
	v_mul_f32_e32 v40, v25, v31
	v_mul_f32_e32 v42, v25, v30
	s_waitcnt vmcnt(11)
	v_mov_b32_e32 v32, v236
	v_mov_b32_e32 v33, v237
	v_mov_b32_e32 v34, v238
	v_mov_b32_e32 v35, v239
	v_pk_mul_f32 v[46:47], v[18:19], v[32:33] op_sel:[1,1] op_sel_hi:[1,0]
	v_mul_f32_e32 v48, v21, v35
	v_mul_f32_e32 v50, v21, v34
	v_pk_mul_f32 v[36:37], v[22:23], v[28:29]
	v_pk_mul_f32 v[44:45], v[18:19], v[32:33]
	v_pk_fma_f32 v[22:23], v[22:23], v[28:29], v[38:39] op_sel_hi:[0,1,1]
	v_pk_fma_f32 v[28:29], v[24:25], v[30:31], v[40:41] op_sel_hi:[1,1,0] neg_lo:[0,0,1] neg_hi:[0,0,1]
	v_pk_fma_f32 v[30:31], v[24:25], v[30:31], v[42:43] op_sel:[0,1,0] op_sel_hi:[1,0,0]
	v_pk_fma_f32 v[18:19], v[18:19], v[32:33], v[46:47] op_sel_hi:[0,1,1]
	v_pk_fma_f32 v[32:33], v[20:21], v[34:35], v[48:49] op_sel_hi:[1,1,0] neg_lo:[0,0,1] neg_hi:[0,0,1]
	v_pk_fma_f32 v[34:35], v[20:21], v[34:35], v[50:51] op_sel:[0,1,0] op_sel_hi:[1,0,0]
	v_sub_f32_e32 v22, v36, v38
	v_sub_f32_e32 v18, v44, v46
	v_mov_b32_e32 v24, v28
	v_mov_b32_e32 v25, v30
	v_mov_b32_e32 v20, v32
	v_mov_b32_e32 v21, v34
; __device__ __forceinline__ u32x4 pack8(f32x4 a, f32x4 b) { u32x4 w; w.x = cvtpk(a[0], a[1]); w.y = cvtpk(a[2], a[3]); w.z = cvtpk(b[0], b[1]); w.w = cvtpk(b[2], b[3]); return w; }
; __device__ __forceinline__ float latent_rstd(const float* ssp, int row, int which) {
;     const f32x4 a = *(const f32x4*)(ssp + ((size_t)row * 2 + which) * 8), b = *(const f32x4*)(ssp + ((size_t)row * 2 + which) * 8 + 4);
;     return 1.0f / sqrtf((((a[0] + a[1]) + (a[2] + a[3])) + ((b[0] + b[1]) + (b[2] + b[3]))) * (1.0f / 512.0f) + 1e-6f);
;     __device__ __forceinline__ void operator()(const Acc& acc, const Unit& u, int wr, int wc, int fr, int fq) const {
;     ...
;             for (int m = 0; m < 4; ++m) { const int row = row0 + ai * HALF + m * 16, pos = row & (SEQ - 1); const float rs = latent_rstd(ssp, row, 0); bf16_t* rowp = O + (size_t)row * ldc + col0;
; #pragma unroll
;                 for (int bj = 0; bj < 2; ++bj) { f32x4 v0 = acc[ai][bj][m][0] * rs, v1 = acc[ai][bj][m][1] * rs; const int d = (col0 + bj * HALF) % 192;
;                     if (d >= 128) { const int jj = (d - 128) >> 1; const f32x4 c01 = rope[pos * 16 + (jj >> 1)], c23 = rope[pos * 16 + (jj >> 1) + 1];
;                         f32x4 w0, w1;
;                         w0[0] = v0[0] * c01[0] - v0[1] * c01[1]; w0[1] = v0[0] * c01[1] + v0[1] * c01[0];
;                         w0[2] = v0[2] * c01[2] - v0[3] * c01[3]; w0[3] = v0[2] * c01[3] + v0[3] * c01[2];
;                         w1[0] = v1[0] * c23[0] - v1[1] * c23[1]; w1[1] = v1[0] * c23[1] + v1[1] * c23[0];
;                         w1[2] = v1[2] * c23[2] - v1[3] * c23[3]; w1[3] = v1[2] * c23[3] + v1[3] * c23[2];
;                         v0 = w0; v1 = w1; }
;                     *(u32x4*)(rowp + bj * HALF) = pack8(v0, v1); } }
.LBB0_1293:
	s_or_b64 exec, exec, s[8:9]
	v_cvt_pk_bf16_f32 v22, v22, v23
	v_cvt_pk_bf16_f32 v23, v24, v25
	v_cvt_pk_bf16_f32 v24, v18, v19
	v_add_u32_e32 v18, 0xb0, v134
	v_ashrrev_i32_e32 v19, 31, v18
	v_cvt_pk_bf16_f32 v25, v20, v21
	v_lshlrev_b64 v[20:21], 6, v[18:19]
	global_store_dwordx4 v[26:27], v[22:25], off offset:256
	s_nop 1
	v_lshl_add_u64 v[24:25], s[10:11], 0, v[20:21]
	s_nop 0
	s_waitcnt vmcnt(8)
	v_mov_b32_e32 v20, v208
	v_mov_b32_e32 v21, v209
	v_mov_b32_e32 v22, v210
	v_mov_b32_e32 v23, v211
	v_mov_b32_e32 v28, v20
	v_mov_b32_e32 v24, v212
	v_mov_b32_e32 v25, v213
	v_mov_b32_e32 v26, v214
	v_mov_b32_e32 v27, v215
	v_mov_b32_e32 v29, v24
	v_mov_b32_e32 v24, v21
	v_mov_b32_e32 v20, v22
	v_mov_b32_e32 v21, v26
	v_mov_b32_e32 v26, v23
	v_pk_add_f32 v[22:23], v[28:29], v[24:25]
	v_pk_add_f32 v[20:21], v[20:21], v[26:27]
	s_nop 0
	v_pk_add_f32 v[20:21], v[22:23], v[20:21]
	s_nop 0
	v_add_f32_e32 v19, v20, v21
	v_fmamk_f32 v19, v19, 0x3b000000, v155
	v_mul_f32_e32 v20, 0x4f800000, v19
	v_cmp_gt_f32_e32 vcc, s89, v19
	v_lshlrev_b32_e32 v21, 4, v18
	s_nop 0
	v_cndmask_b32_e32 v19, v19, v20, vcc
	v_sqrt_f32_e32 v20, v19
	s_nop 0
	v_add_u32_e32 v22, -1, v20
	v_add_u32_e32 v23, 1, v20
	v_fma_f32 v24, -v22, v20, v19
	v_fma_f32 v25, -v23, v20, v19
	v_cmp_ge_f32_e64 s[8:9], 0, v24
	s_nop 1
	v_cndmask_b32_e64 v20, v20, v22, s[8:9]
	v_cmp_lt_f32_e64 s[8:9], 0, v25
	s_nop 1
	v_cndmask_b32_e64 v20, v20, v23, s[8:9]
	v_mul_f32_e32 v22, 0x37800000, v20
	v_cndmask_b32_e32 v20, v20, v22, vcc
	v_cmp_class_f32_e32 vcc, v19, v156
	s_nop 1
	v_cndmask_b32_e32 v20, v20, v19, vcc
	v_div_scale_f32 v22, s[8:9], v20, v20, 1.0
	v_rcp_f32_e32 v23, v22
	v_and_b32_e32 v19, 0xfff0, v21
	v_div_scale_f32 v21, vcc, 1.0, v20, 1.0
	v_fma_f32 v24, -v22, v23, 1.0
	v_fmac_f32_e32 v23, v24, v23
	v_mul_f32_e32 v24, v21, v23
	v_fma_f32 v25, -v22, v24, v21
	v_fmac_f32_e32 v24, v25, v23
	v_fma_f32 v21, -v22, v24, v21
	v_div_fmas_f32 v21, v21, v23, v24
	v_div_fixup_f32 v20, v21, v20, 1.0
	v_pk_mul_f32 v[16:17], v[16:17], v[20:21] op_sel_hi:[1,0]
	v_pk_mul_f32 v[14:15], v[14:15], v[20:21] op_sel_hi:[1,0]
	v_pk_mul_f32 v[22:23], v[12:13], v[20:21] op_sel_hi:[1,0]
	v_pk_mul_f32 v[12:13], v[10:11], v[20:21] op_sel_hi:[1,0]
	s_and_saveexec_b64 s[8:9], s[4:5]
	s_cbranch_execz .LBB0_1295
	v_add_u32_e32 v130, v135, v19
	v_lshl_add_u64 v[10:11], v[130:131], 4, s[38:39]
	s_waitcnt vmcnt(7)
	v_mov_b32_e32 v24, v240
	v_mov_b32_e32 v25, v241
	v_mov_b32_e32 v26, v242
	v_mov_b32_e32 v27, v243
	v_pk_mul_f32 v[32:33], v[14:15], v[24:25] op_sel:[1,1] op_sel_hi:[1,0]
	v_mul_f32_e32 v34, v17, v27
	v_mul_f32_e32 v36, v17, v26
	s_waitcnt vmcnt(6)
	v_mov_b32_e32 v28, v244
	v_mov_b32_e32 v29, v245
	v_mov_b32_e32 v30, v246
	v_mov_b32_e32 v31, v247
	v_pk_mul_f32 v[40:41], v[12:13], v[28:29] op_sel:[1,1] op_sel_hi:[1,0]
	v_mul_f32_e32 v42, v23, v31
	v_mul_f32_e32 v44, v23, v30
	v_pk_mul_f32 v[10:11], v[14:15], v[24:25]
	v_pk_mul_f32 v[38:39], v[12:13], v[28:29]
	v_pk_fma_f32 v[14:15], v[14:15], v[24:25], v[32:33] op_sel_hi:[0,1,1]
	v_pk_fma_f32 v[24:25], v[16:17], v[26:27], v[34:35] op_sel_hi:[1,1,0] neg_lo:[0,0,1] neg_hi:[0,0,1]
	v_pk_fma_f32 v[26:27], v[16:17], v[26:27], v[36:37] op_sel:[0,1,0] op_sel_hi:[1,0,0]
	v_pk_fma_f32 v[12:13], v[12:13], v[28:29], v[40:41] op_sel_hi:[0,1,1]
	v_pk_fma_f32 v[28:29], v[22:23], v[30:31], v[42:43] op_sel_hi:[1,1,0] neg_lo:[0,0,1] neg_hi:[0,0,1]
	v_pk_fma_f32 v[30:31], v[22:23], v[30:31], v[44:45] op_sel:[0,1,0] op_sel_hi:[1,0,0]
	v_sub_f32_e32 v14, v10, v32
	v_sub_f32_e32 v12, v38, v40
	v_mov_b32_e32 v16, v24
	v_mov_b32_e32 v17, v26
	v_mov_b32_e32 v22, v28
	v_mov_b32_e32 v23, v30
.LBB0_1295:
	s_or_b64 exec, exec, s[8:9]
	v_mov_b64_e32 v[10:11], s[30:31]
	v_mov_b32_e32 v21, v20
	v_mad_i64_i32 v[10:11], s[4:5], v18, s92, v[10:11]
	v_cvt_pk_bf16_f32 v14, v14, v15
	v_cvt_pk_bf16_f32 v15, v16, v17
	v_cvt_pk_bf16_f32 v16, v12, v13
	v_mov_b32_e32 v12, v20
	v_mov_b32_e32 v13, v20
	v_lshl_add_u64 v[10:11], v[132:133], 1, v[10:11]
	v_pk_mul_f32 v[8:9], v[8:9], v[12:13]
	v_pk_mul_f32 v[6:7], v[6:7], v[20:21]
	v_pk_mul_f32 v[4:5], v[4:5], v[12:13]
	v_pk_mul_f32 v[2:3], v[2:3], v[20:21]
	v_cvt_pk_bf16_f32 v17, v22, v23
	global_store_dwordx4 v[10:11], v[14:17], off
	s_and_saveexec_b64 s[4:5], s[6:7]
	s_cbranch_execz .LBB0_1297
	v_add_u32_e32 v130, v124, v19
	v_lshl_add_u64 v[16:17], v[130:131], 4, s[38:39]
	s_waitcnt vmcnt(8)
	v_mov_b32_e32 v12, v240
	v_mov_b32_e32 v13, v241
	v_mov_b32_e32 v14, v242
	v_mov_b32_e32 v15, v243
	v_pk_mul_f32 v[22:23], v[6:7], v[12:13] op_sel:[1,1] op_sel_hi:[1,0]
	v_mul_f32_e32 v24, v9, v15
	v_mul_f32_e32 v26, v9, v14
	s_waitcnt vmcnt(7)
	v_mov_b32_e32 v16, v244
	v_mov_b32_e32 v17, v245
	v_mov_b32_e32 v18, v246
	v_mov_b32_e32 v19, v247
	v_pk_mul_f32 v[30:31], v[2:3], v[16:17] op_sel:[1,1] op_sel_hi:[1,0]
	v_mul_f32_e32 v32, v5, v19
	v_mul_f32_e32 v34, v5, v18
	v_pk_mul_f32 v[20:21], v[6:7], v[12:13]
	v_pk_mul_f32 v[28:29], v[2:3], v[16:17]
	v_pk_fma_f32 v[6:7], v[6:7], v[12:13], v[22:23] op_sel_hi:[0,1,1]
	v_pk_fma_f32 v[12:13], v[8:9], v[14:15], v[24:25] op_sel_hi:[1,1,0] neg_lo:[0,0,1] neg_hi:[0,0,1]
	v_pk_fma_f32 v[14:15], v[8:9], v[14:15], v[26:27] op_sel:[0,1,0] op_sel_hi:[1,0,0]
	v_pk_fma_f32 v[2:3], v[2:3], v[16:17], v[30:31] op_sel_hi:[0,1,1]
	v_pk_fma_f32 v[16:17], v[4:5], v[18:19], v[32:33] op_sel_hi:[1,1,0] neg_lo:[0,0,1] neg_hi:[0,0,1]
	v_pk_fma_f32 v[18:19], v[4:5], v[18:19], v[34:35] op_sel:[0,1,0] op_sel_hi:[1,0,0]
	v_sub_f32_e32 v6, v20, v22
	v_sub_f32_e32 v2, v28, v30
	v_mov_b32_e32 v8, v12
	v_mov_b32_e32 v9, v14
	v_mov_b32_e32 v4, v16
	v_mov_b32_e32 v5, v18
